# v16 + K-loop heads (regular and peeled first-trip copies) aligned to 64 bytes
# speedup vs baseline: 1.0019x; 1.0019x over previous
.LBB0_248:
	s_xor_b64 s[10:11], s[30:31], -1
	s_and_b64 s[20:21], s[30:31], exec
	s_cselect_b32 s3, s7, s27
	s_cselect_b32 s5, s6, s26
	s_cselect_b32 s20, s9, s47
	s_cselect_b32 s21, s8, s46
	s_add_u32 s26, s26, 0x40080
	s_addc_u32 s27, s27, 0
	s_add_u32 s22, s46, 0x100
	v_mov_b32_e32 v2, 0
	s_addc_u32 s25, s47, 0
	s_mov_b32 s30, -2
	.p2align 6
.Lpeel_0:
	s_add_u32 s31, s26, 0xfffc0080
	s_addc_u32 s33, s27, -1
	s_add_i32 s34, 0, 0x10000
	v_add_u32_e32 v0, s34, v138
	ds_read_b128 v[140:143], v0
	ds_read_b128 v[144:147], v0 offset:1024
	ds_read_b128 v[148:151], v0 offset:2048
	ds_read_b128 v[152:155], v0 offset:3072
	s_cmp_eq_u32 s30, 12
	s_cselect_b32 s49, s3, s33
	s_cselect_b32 s48, s5, s31
	s_cselect_b32 s47, s20, s25
	s_cselect_b32 s46, s21, s22
	v_mov_b32_e32 v0, v136
	ds_read_b128 v[156:159], v139
	ds_read_b128 v[160:163], v139 offset:1024
	ds_read_b128 v[172:175], v139 offset:2048
	ds_read_b128 v[176:179], v139 offset:3072
	ds_read_b128 v[180:183], v139 offset:4096
	ds_read_b128 v[184:187], v139 offset:5120
	ds_read_b128 v[188:191], v139 offset:6144
	ds_read_b128 v[192:195], v139 offset:7168
	s_nop 0
	v_mov_b32_e32 v0, v137
	s_nop 0
	s_waitcnt lgkmcnt(8)
	s_barrier
	s_waitcnt lgkmcnt(0)
	s_setprio 1
	v_mov_b64_e32 v[50:51], v[164:165]
	s_waitcnt lgkmcnt(0)
	v_mfma_scale_f32_16x16x128_f8f6f4 v[98:101], v[156:163], v[148:155], 0, v202, v202 op_sel_hi:[0,0,0]
	v_mov_b64_e32 v[52:53], v[166:167]
	v_mfma_scale_f32_16x16x128_f8f6f4 v[164:167], v[172:179], v[140:147], 0, v202, v202 op_sel_hi:[0,0,0]
	s_add_i32 m0, s1, 0xc000
	v_mfma_scale_f32_16x16x128_f8f6f4 v[90:93], v[180:187], v[148:155], 0, v202, v202 op_sel_hi:[0,0,0]
	global_load_lds_dwordx4 v136, s[26:27]
	v_mfma_scale_f32_16x16x128_f8f6f4 v[130:133], v[156:163], v[140:147], 0, v202, v202 op_sel_hi:[0,0,0]
	v_mfma_scale_f32_16x16x128_f8f6f4 v[168:171], v[172:179], v[148:155], 0, v202, v202 op_sel_hi:[0,0,0]
	s_add_i32 m0, s1, 0xe000
	v_mfma_scale_f32_16x16x128_f8f6f4 v[196:199], v[180:187], v[140:147], 0, v202, v202 op_sel_hi:[0,0,0]
	global_load_lds_dwordx4 v137, s[26:27]
	v_mfma_scale_f32_16x16x128_f8f6f4 v[206:209], v[188:195], v[140:147], 0, v202, v202 op_sel_hi:[0,0,0]
	v_mfma_scale_f32_16x16x128_f8f6f4 v[210:213], v[188:195], v[148:155], 0, v202, v202 op_sel_hi:[0,0,0]
	s_setprio 0
	s_barrier
	s_add_i32 s31, 0, 0x14000
	v_add_u32_e32 v0, s31, v138
	s_nop 2
	ds_read_b128 v[82:85], v0
	ds_read_b128 v[86:89], v0 offset:1024
	ds_read_b128 v[114:117], v0 offset:2048
	ds_read_b128 v[118:121], v0 offset:3072
	v_mov_b32_e32 v0, v136
	s_add_i32 s33, s34, s73
	s_nop 0
	v_mov_b32_e32 v0, v137
	s_nop 0
	s_barrier
	s_waitcnt lgkmcnt(0)
	s_setprio 1
	s_waitcnt lgkmcnt(0)
	v_mfma_scale_f32_16x16x128_f8f6f4 v[66:69], v[156:163], v[82:89], 0, v202, v202 op_sel_hi:[0,0,0]
	v_mfma_scale_f32_16x16x128_f8f6f4 v[38:41], v[156:163], v[114:121], 0, v202, v202 op_sel_hi:[0,0,0]
	s_mov_b32 m0, s33
	v_mfma_scale_f32_16x16x128_f8f6f4 v[58:61], v[180:187], v[82:89], 0, v202, v202 op_sel_hi:[0,0,0]
	global_load_lds_dwordx4 v136, s[46:47]
	v_mfma_scale_f32_16x16x128_f8f6f4 v[214:217], v[172:179], v[82:89], 0, v202, v202 op_sel_hi:[0,0,0]
	v_mfma_scale_f32_16x16x128_f8f6f4 v[172:175], v[172:179], v[114:121], 0, v202, v202 op_sel_hi:[0,0,0]
	s_add_i32 m0, s33, 0x2000
	v_mfma_scale_f32_16x16x128_f8f6f4 v[176:179], v[180:187], v[114:121], 0, v202, v202 op_sel_hi:[0,0,0]
	global_load_lds_dwordx4 v137, s[46:47]
	v_mfma_scale_f32_16x16x128_f8f6f4 v[180:183], v[188:195], v[82:89], 0, v202, v202 op_sel_hi:[0,0,0]
	v_mfma_scale_f32_16x16x128_f8f6f4 v[184:187], v[188:195], v[114:121], 0, v202, v202 op_sel_hi:[0,0,0]
	s_setprio 0
	v_mov_b32_e32 v0, v136
	s_barrier
	s_nop 1
	ds_read_b128 v[18:21], v139 offset:16384
	ds_read_b128 v[22:25], v139 offset:17408
	ds_read_b128 v[50:53], v139 offset:18432
	ds_read_b128 v[54:57], v139 offset:19456
	ds_read_b128 v[122:125], v139 offset:20480
	ds_read_b128 v[126:129], v139 offset:21504
	ds_read_b128 v[156:159], v139 offset:22528
	ds_read_b128 v[160:163], v139 offset:23552
	s_nop 0
	v_mov_b32_e32 v0, v137
	s_nop 0
	s_barrier
	s_waitcnt lgkmcnt(0)
	s_setprio 1
	s_waitcnt lgkmcnt(0)
	v_mfma_scale_f32_16x16x128_f8f6f4 v[110:113], v[18:25], v[140:147], 0, v202, v202 op_sel_hi:[0,0,0]
	v_mfma_scale_f32_16x16x128_f8f6f4 v[78:81], v[18:25], v[148:155], 0, v202, v202 op_sel_hi:[0,0,0]
	s_mov_b32 m0, s1
	v_mfma_scale_f32_16x16x128_f8f6f4 v[102:105], v[50:57], v[140:147], 0, v202, v202 op_sel_hi:[0,0,0]
	global_load_lds_dwordx4 v136, s[48:49]
	v_mfma_scale_f32_16x16x128_f8f6f4 v[106:109], v[122:129], v[140:147], 0, v202, v202 op_sel_hi:[0,0,0]
	v_mfma_scale_f32_16x16x128_f8f6f4 v[94:97], v[156:163], v[140:147], 0, v202, v202 op_sel_hi:[0,0,0]
	s_mov_b32 m0, s13
	v_mfma_scale_f32_16x16x128_f8f6f4 v[62:65], v[156:163], v[148:155], 0, v202, v202 op_sel_hi:[0,0,0]
	global_load_lds_dwordx4 v137, s[48:49]
	v_mfma_scale_f32_16x16x128_f8f6f4 v[218:221], v[50:57], v[148:155], 0, v202, v202 op_sel_hi:[0,0,0]
	v_mfma_scale_f32_16x16x128_f8f6f4 v[222:225], v[122:129], v[148:155], 0, v202, v202 op_sel_hi:[0,0,0]
	s_setprio 0
	s_barrier
	s_add_u32 s34, s46, 0x40000
	s_addc_u32 s35, s47, 0
	v_mov_b32_e32 v0, v136
	s_add_i32 s31, s31, s73
	s_mov_b32 s100, s31
	s_nop 0
	v_mov_b32_e32 v0, v137
	s_add_i32 s101, s31, 0x2000
	s_nop 0
	s_waitcnt vmcnt(4)
	s_barrier
	s_setprio 1
	v_mfma_scale_f32_16x16x128_f8f6f4 v[34:37], v[50:57], v[82:89], 0, v202, v202 op_sel_hi:[0,0,0]
	v_mfma_scale_f32_16x16x128_f8f6f4 v[226:229], v[18:25], v[82:89], 0, v202, v202 op_sel_hi:[0,0,0]
	s_mov_b32 m0, s100
	v_mfma_scale_f32_16x16x128_f8f6f4 v[230:233], v[18:25], v[114:121], 0, v202, v202 op_sel_hi:[0,0,0]
	global_load_lds_dwordx4 v136, s[34:35]
	v_mfma_scale_f32_16x16x128_f8f6f4 v[234:237], v[50:57], v[114:121], 0, v202, v202 op_sel_hi:[0,0,0]
	v_mfma_scale_f32_16x16x128_f8f6f4 v[238:241], v[122:129], v[82:89], 0, v202, v202 op_sel_hi:[0,0,0]
	s_mov_b32 m0, s101
	v_mfma_scale_f32_16x16x128_f8f6f4 v[242:245], v[122:129], v[114:121], 0, v202, v202 op_sel_hi:[0,0,0]
	global_load_lds_dwordx4 v137, s[34:35]
	v_mfma_scale_f32_16x16x128_f8f6f4 v[246:249], v[156:163], v[82:89], 0, v202, v202 op_sel_hi:[0,0,0]
	v_mfma_scale_f32_16x16x128_f8f6f4 v[50:53], v[156:163], v[114:121], 0, v202, v202 op_sel_hi:[0,0,0]
	s_setprio 0
	s_add_i32 s31, 0, 0x18000
	v_add_u32_e32 v0, s31, v138
	s_barrier
	s_nop 2
	ds_read_b128 v[2:5], v0
	ds_read_b128 v[6:9], v0 offset:1024
	ds_read_b128 v[10:13], v0 offset:2048
	ds_read_b128 v[14:17], v0 offset:3072
	s_add_u32 s34, s48, 0x40000
	v_mov_b32_e32 v0, v136
	ds_read_b128 v[18:21], v139 offset:32768
	ds_read_b128 v[22:25], v139 offset:33792
	ds_read_b128 v[26:29], v139 offset:34816
	ds_read_b128 v[30:33], v139 offset:35840
	ds_read_b128 v[42:45], v139 offset:36864
	ds_read_b128 v[46:49], v139 offset:37888
	ds_read_b128 v[70:73], v139 offset:38912
	ds_read_b128 v[74:77], v139 offset:39936
	s_addc_u32 s35, s49, 0
	s_nop 0
	v_mov_b32_e32 v0, v137
	s_nop 0
	s_waitcnt lgkmcnt(8)
	s_barrier
	s_waitcnt lgkmcnt(0)
	s_setprio 1
	s_waitcnt lgkmcnt(0)
	v_mfma_scale_f32_16x16x128_f8f6f4 v[126:129], v[18:25], v[2:9], v[130:133], v202, v202 op_sel_hi:[0,0,0]
	v_mfma_scale_f32_16x16x128_f8f6f4 v[98:101], v[18:25], v[10:17], v[98:101], v202, v202 op_sel_hi:[0,0,0]
	s_mov_b32 m0, s14
	v_mfma_scale_f32_16x16x128_f8f6f4 v[118:121], v[26:33], v[2:9], v[164:167], v202, v202 op_sel_hi:[0,0,0]
	global_load_lds_dwordx4 v136, s[34:35]
	v_mfma_scale_f32_16x16x128_f8f6f4 v[86:89], v[26:33], v[10:17], v[168:171], v202, v202 op_sel_hi:[0,0,0]
	v_mfma_scale_f32_16x16x128_f8f6f4 v[122:125], v[42:49], v[2:9], v[196:199], v202, v202 op_sel_hi:[0,0,0]
	s_mov_b32 m0, s15
	v_mfma_scale_f32_16x16x128_f8f6f4 v[90:93], v[42:49], v[10:17], v[90:93], v202, v202 op_sel_hi:[0,0,0]
	global_load_lds_dwordx4 v137, s[34:35]
	v_mfma_scale_f32_16x16x128_f8f6f4 v[114:117], v[70:77], v[2:9], v[206:209], v202, v202 op_sel_hi:[0,0,0]
	v_mfma_scale_f32_16x16x128_f8f6f4 v[82:85], v[70:77], v[10:17], v[210:213], v202, v202 op_sel_hi:[0,0,0]
	s_setprio 0
	s_barrier
	s_add_i32 s33, 0, 0x1c000
	v_add_u32_e32 v0, s33, v138
	ds_read_b128 v[140:143], v0
	ds_read_b128 v[144:147], v0 offset:1024
	ds_read_b128 v[148:151], v0 offset:2048
	ds_read_b128 v[152:155], v0 offset:3072
	v_mov_b32_e32 v0, v136
	s_add_i32 s31, s31, s73
	v_lshl_add_u64 v[54:55], s[46:47], 0, v[0:1]
	v_lshl_add_u64 v[54:55], v[54:55], 0, s[66:67]
	v_mov_b32_e32 v0, v137
	v_lshl_add_u64 v[54:55], s[46:47], 0, v[0:1]
	v_lshl_add_u64 v[54:55], v[54:55], 0, s[66:67]
	s_barrier
	s_waitcnt lgkmcnt(0)
	s_setprio 1
	s_waitcnt lgkmcnt(0)
	v_mfma_scale_f32_16x16x128_f8f6f4 v[66:69], v[18:25], v[140:147], v[66:69], v202, v202 op_sel_hi:[0,0,0]
	v_mfma_scale_f32_16x16x128_f8f6f4 v[38:41], v[18:25], v[148:155], v[38:41], v202, v202 op_sel_hi:[0,0,0]
	s_add_u32 s98, s46, s66
	s_addc_u32 s99, s47, s67
	s_mov_b32 m0, s31
	v_mfma_scale_f32_16x16x128_f8f6f4 v[54:57], v[26:33], v[140:147], v[214:217], v202, v202 op_sel_hi:[0,0,0]
	global_load_lds_dwordx4 v136, s[98:99]
	v_mfma_scale_f32_16x16x128_f8f6f4 v[22:25], v[26:33], v[148:155], v[172:175], v202, v202 op_sel_hi:[0,0,0]
	v_mfma_scale_f32_16x16x128_f8f6f4 v[58:61], v[42:49], v[140:147], v[58:61], v202, v202 op_sel_hi:[0,0,0]
	s_add_i32 m0, s31, 0x2000
	v_mfma_scale_f32_16x16x128_f8f6f4 v[30:33], v[42:49], v[148:155], v[176:179], v202, v202 op_sel_hi:[0,0,0]
	global_load_lds_dwordx4 v137, s[98:99]
	v_mfma_scale_f32_16x16x128_f8f6f4 v[18:21], v[70:77], v[140:147], v[180:183], v202, v202 op_sel_hi:[0,0,0]
	v_mfma_scale_f32_16x16x128_f8f6f4 v[164:167], v[70:77], v[148:155], v[184:187], v202, v202 op_sel_hi:[0,0,0]
	s_setprio 0
	v_mov_b32_e32 v0, v136
	s_barrier
	ds_read_b128 v[156:159], v139 offset:49152
	ds_read_b128 v[160:163], v139 offset:50176
	ds_read_b128 v[172:175], v139 offset:51200
	ds_read_b128 v[176:179], v139 offset:52224
	ds_read_b128 v[180:183], v139 offset:53248
	ds_read_b128 v[184:187], v139 offset:54272
	ds_read_b128 v[188:191], v139 offset:55296
	ds_read_b128 v[192:195], v139 offset:56320
	v_lshl_add_u64 v[26:27], s[48:49], 0, v[0:1]
	v_lshl_add_u64 v[26:27], v[26:27], 0, s[66:67]
	v_mov_b32_e32 v0, v137
	v_lshl_add_u64 v[26:27], s[48:49], 0, v[0:1]
	v_lshl_add_u64 v[26:27], v[26:27], 0, s[66:67]
	s_barrier
	s_waitcnt lgkmcnt(0)
	s_setprio 1
	s_waitcnt lgkmcnt(0)
	v_mfma_scale_f32_16x16x128_f8f6f4 v[110:113], v[156:163], v[2:9], v[110:113], v202, v202 op_sel_hi:[0,0,0]
	v_mfma_scale_f32_16x16x128_f8f6f4 v[78:81], v[156:163], v[10:17], v[78:81], v202, v202 op_sel_hi:[0,0,0]
	s_add_u32 s98, s48, s66
	s_addc_u32 s99, s49, s67
	s_mov_b32 m0, s17
	v_mfma_scale_f32_16x16x128_f8f6f4 v[102:105], v[172:179], v[2:9], v[102:105], v202, v202 op_sel_hi:[0,0,0]
	global_load_lds_dwordx4 v136, s[98:99]
	v_mfma_scale_f32_16x16x128_f8f6f4 v[70:73], v[172:179], v[10:17], v[218:221], v202, v202 op_sel_hi:[0,0,0]
	v_mfma_scale_f32_16x16x128_f8f6f4 v[106:109], v[180:187], v[2:9], v[106:109], v202, v202 op_sel_hi:[0,0,0]
	s_mov_b32 m0, s18
	v_mfma_scale_f32_16x16x128_f8f6f4 v[74:77], v[180:187], v[10:17], v[222:225], v202, v202 op_sel_hi:[0,0,0]
	global_load_lds_dwordx4 v137, s[98:99]
	v_mfma_scale_f32_16x16x128_f8f6f4 v[94:97], v[188:195], v[2:9], v[94:97], v202, v202 op_sel_hi:[0,0,0]
	v_mfma_scale_f32_16x16x128_f8f6f4 v[62:65], v[188:195], v[10:17], v[62:65], v202, v202 op_sel_hi:[0,0,0]
	s_setprio 0
	s_barrier
	s_add_u32 s34, s46, 0x40080
	s_addc_u32 s35, s47, 0
	v_mov_b32_e32 v0, v136
	s_add_i32 s31, s33, s73
	s_nop 0
	v_mov_b32_e32 v0, v137
	s_nop 0
	s_waitcnt vmcnt(4)
	s_barrier
	s_setprio 1
	v_mfma_scale_f32_16x16x128_f8f6f4 v[46:49], v[156:163], v[140:147], v[226:229], v202, v202 op_sel_hi:[0,0,0]
	v_mfma_scale_f32_16x16x128_f8f6f4 v[14:17], v[156:163], v[148:155], v[230:233], v202, v202 op_sel_hi:[0,0,0]
	s_mov_b32 m0, s31
	v_mfma_scale_f32_16x16x128_f8f6f4 v[34:37], v[172:179], v[140:147], v[34:37], v202, v202 op_sel_hi:[0,0,0]
	global_load_lds_dwordx4 v136, s[34:35]
	v_mfma_scale_f32_16x16x128_f8f6f4 v[6:9], v[172:179], v[148:155], v[234:237], v202, v202 op_sel_hi:[0,0,0]
	v_mfma_scale_f32_16x16x128_f8f6f4 v[42:45], v[180:187], v[140:147], v[238:241], v202, v202 op_sel_hi:[0,0,0]
	s_add_i32 m0, s31, 0x2000
	v_mfma_scale_f32_16x16x128_f8f6f4 v[10:13], v[180:187], v[148:155], v[242:245], v202, v202 op_sel_hi:[0,0,0]
	global_load_lds_dwordx4 v137, s[34:35]
	v_mfma_scale_f32_16x16x128_f8f6f4 v[26:29], v[188:195], v[140:147], v[246:249], v202, v202 op_sel_hi:[0,0,0]
	v_mfma_scale_f32_16x16x128_f8f6f4 v[2:5], v[188:195], v[148:155], v[50:53], v202, v202 op_sel_hi:[0,0,0]
	s_setprio 0
	s_add_i32 s30, s30, 2
	s_add_u32 s26, s26, 0x100
	s_addc_u32 s27, s27, 0
	s_add_u32 s22, s22, 0x100
	s_addc_u32 s25, s25, 0
	s_cmp_gt_u32 s30, 13
	s_barrier
	s_cbranch_scc0 .LBB0_249
	s_branch .Lpeel_exit_0
	.p2align 6

.LBB0_277:
	s_xor_b64 s[56:57], s[10:11], -1
	s_and_b64 s[10:11], s[10:11], exec
	s_cselect_b32 s3, s53, s5
	s_cselect_b32 s9, s52, s4
	s_cselect_b32 s12, s55, s7
	s_cselect_b32 s13, s54, s6
	s_add_u32 s4, s4, 0x40080
	s_addc_u32 s5, s5, 0
	s_add_u32 s15, s6, 0x100
	s_waitcnt lgkmcnt(0)
	v_mov_b32_e32 v4, 0
	s_addc_u32 s16, s7, 0
	s_mov_b32 s17, -2
	.p2align 6
.Lpeel_1:
	s_add_u32 s6, s4, 0xfffc0080
	s_addc_u32 s7, s5, -1
	s_add_i32 s25, 0, 0x10000
	v_add_u32_e32 v0, s25, v207
	ds_read_b128 v[52:55], v0
	ds_read_b128 v[56:59], v0 offset:1024
	ds_read_b128 v[68:71], v0 offset:2048
	ds_read_b128 v[72:75], v0 offset:3072
	s_cmp_eq_u32 s17, 12
	s_cselect_b32 s11, s3, s7
	s_cselect_b32 s10, s9, s6
	s_cselect_b32 s7, s12, s16
	s_cselect_b32 s6, s13, s15
	v_mov_b32_e32 v0, v205
	ds_read_b128 v[84:87], v208
	ds_read_b128 v[88:91], v208 offset:1024
	ds_read_b128 v[92:95], v208 offset:2048
	ds_read_b128 v[96:99], v208 offset:3072
	ds_read_b128 v[172:175], v208 offset:4096
	ds_read_b128 v[176:179], v208 offset:5120
	ds_read_b128 v[180:183], v208 offset:6144
	ds_read_b128 v[184:187], v208 offset:7168
	s_nop 0
	v_mov_b32_e32 v0, v206
	s_nop 0
	s_waitcnt lgkmcnt(8)
	s_barrier
	s_waitcnt lgkmcnt(0)
	s_setprio 1
	s_waitcnt lgkmcnt(0)
	v_mfma_scale_f32_16x16x128_f8f6f4 v[164:167], v[52:59], v[84:91], 0, v202, v202 op_sel_hi:[0,0,0]
	v_mfma_scale_f32_16x16x128_f8f6f4 v[160:163], v[68:75], v[84:91], 0, v202, v202 op_sel_hi:[0,0,0]
	s_add_i32 m0, s18, 0xc000
	v_mfma_scale_f32_16x16x128_f8f6f4 v[156:159], v[52:59], v[92:99], 0, v202, v202 op_sel_hi:[0,0,0]
	global_load_lds_dwordx4 v205, s[4:5]
	v_mfma_scale_f32_16x16x128_f8f6f4 v[152:155], v[68:75], v[92:99], 0, v202, v202 op_sel_hi:[0,0,0]
	v_mfma_scale_f32_16x16x128_f8f6f4 v[148:151], v[52:59], v[172:179], 0, v202, v202 op_sel_hi:[0,0,0]
	s_add_i32 m0, s18, 0xe000
	v_mfma_scale_f32_16x16x128_f8f6f4 v[188:191], v[68:75], v[172:179], 0, v202, v202 op_sel_hi:[0,0,0]
	global_load_lds_dwordx4 v206, s[4:5]
	v_mfma_scale_f32_16x16x128_f8f6f4 v[192:195], v[52:59], v[180:187], 0, v202, v202 op_sel_hi:[0,0,0]
	v_mfma_scale_f32_16x16x128_f8f6f4 v[196:199], v[68:75], v[180:187], 0, v202, v202 op_sel_hi:[0,0,0]
	s_setprio 0
	s_barrier
	s_add_i32 s30, 0, 0x14000
	v_add_u32_e32 v0, s30, v207
	s_nop 2
	ds_read_b128 v[132:135], v0
	ds_read_b128 v[136:139], v0 offset:1024
	ds_read_b128 v[140:143], v0 offset:2048
	ds_read_b128 v[144:147], v0 offset:3072
	v_mov_b32_e32 v0, v205
	s_add_i32 s25, s25, s73
	s_nop 0
	v_mov_b32_e32 v0, v206
	s_nop 0
	s_barrier
	s_waitcnt lgkmcnt(0)
	s_setprio 1
	s_waitcnt lgkmcnt(0)
	v_mfma_scale_f32_16x16x128_f8f6f4 v[128:131], v[132:139], v[84:91], 0, v202, v202 op_sel_hi:[0,0,0]
	v_mfma_scale_f32_16x16x128_f8f6f4 v[124:127], v[140:147], v[84:91], 0, v202, v202 op_sel_hi:[0,0,0]
	s_mov_b32 m0, s25
	v_mfma_scale_f32_16x16x128_f8f6f4 v[120:123], v[132:139], v[92:99], 0, v202, v202 op_sel_hi:[0,0,0]
	global_load_lds_dwordx4 v205, s[6:7]
	v_mfma_scale_f32_16x16x128_f8f6f4 v[116:119], v[140:147], v[92:99], 0, v202, v202 op_sel_hi:[0,0,0]
	v_mfma_scale_f32_16x16x128_f8f6f4 v[210:213], v[132:139], v[172:179], 0, v202, v202 op_sel_hi:[0,0,0]
	s_add_i32 m0, s25, 0x2000
	v_mfma_scale_f32_16x16x128_f8f6f4 v[172:175], v[140:147], v[172:179], 0, v202, v202 op_sel_hi:[0,0,0]
	global_load_lds_dwordx4 v206, s[6:7]
	v_mfma_scale_f32_16x16x128_f8f6f4 v[176:179], v[132:139], v[180:187], 0, v202, v202 op_sel_hi:[0,0,0]
	v_mfma_scale_f32_16x16x128_f8f6f4 v[180:183], v[140:147], v[180:187], 0, v202, v202 op_sel_hi:[0,0,0]
	s_setprio 0
	v_mov_b32_e32 v0, v205
	s_barrier
	ds_read_b128 v[84:87], v208 offset:16384
	ds_read_b128 v[88:91], v208 offset:17408
	ds_read_b128 v[92:95], v208 offset:18432
	ds_read_b128 v[96:99], v208 offset:19456
	ds_read_b128 v[100:103], v208 offset:20480
	ds_read_b128 v[104:107], v208 offset:21504
	ds_read_b128 v[108:111], v208 offset:22528
	ds_read_b128 v[112:115], v208 offset:23552
	s_nop 0
	v_mov_b32_e32 v0, v206
	s_nop 0
	s_barrier
	s_waitcnt lgkmcnt(0)
	s_setprio 1
	s_waitcnt lgkmcnt(0)
	v_mfma_scale_f32_16x16x128_f8f6f4 v[80:83], v[52:59], v[84:91], 0, v202, v202 op_sel_hi:[0,0,0]
	v_mfma_scale_f32_16x16x128_f8f6f4 v[76:79], v[68:75], v[84:91], 0, v202, v202 op_sel_hi:[0,0,0]
	s_mov_b32 m0, s18
	v_mfma_scale_f32_16x16x128_f8f6f4 v[64:67], v[52:59], v[92:99], 0, v202, v202 op_sel_hi:[0,0,0]
	global_load_lds_dwordx4 v205, s[10:11]
	v_mfma_scale_f32_16x16x128_f8f6f4 v[60:63], v[68:75], v[92:99], 0, v202, v202 op_sel_hi:[0,0,0]
	v_mfma_scale_f32_16x16x128_f8f6f4 v[184:187], v[52:59], v[100:107], 0, v202, v202 op_sel_hi:[0,0,0]
	s_mov_b32 m0, s19
	v_mfma_scale_f32_16x16x128_f8f6f4 v[214:217], v[68:75], v[100:107], 0, v202, v202 op_sel_hi:[0,0,0]
	global_load_lds_dwordx4 v206, s[10:11]
	v_mfma_scale_f32_16x16x128_f8f6f4 v[218:221], v[52:59], v[108:115], 0, v202, v202 op_sel_hi:[0,0,0]
	v_mfma_scale_f32_16x16x128_f8f6f4 v[222:225], v[68:75], v[108:115], 0, v202, v202 op_sel_hi:[0,0,0]
	s_setprio 0
	s_barrier
	s_add_u32 s26, s6, 0x40000
	s_addc_u32 s27, s7, 0
	v_mov_b32_e32 v0, v205
	s_add_i32 s25, s30, s73
	s_mov_b32 s100, s25
	s_nop 0
	v_mov_b32_e32 v0, v206
	s_add_i32 s101, s25, 0x2000
	s_nop 0
	s_waitcnt vmcnt(4)
	s_barrier
	s_setprio 1
	v_mfma_scale_f32_16x16x128_f8f6f4 v[226:229], v[132:139], v[84:91], 0, v202, v202 op_sel_hi:[0,0,0]
	v_mfma_scale_f32_16x16x128_f8f6f4 v[230:233], v[140:147], v[84:91], 0, v202, v202 op_sel_hi:[0,0,0]
	s_mov_b32 m0, s100
	v_mfma_scale_f32_16x16x128_f8f6f4 v[234:237], v[132:139], v[92:99], 0, v202, v202 op_sel_hi:[0,0,0]
	global_load_lds_dwordx4 v205, s[26:27]
	v_mfma_scale_f32_16x16x128_f8f6f4 v[238:241], v[140:147], v[92:99], 0, v202, v202 op_sel_hi:[0,0,0]
	v_mfma_scale_f32_16x16x128_f8f6f4 v[242:245], v[132:139], v[100:107], 0, v202, v202 op_sel_hi:[0,0,0]
	s_mov_b32 m0, s101
	v_mfma_scale_f32_16x16x128_f8f6f4 v[246:249], v[140:147], v[100:107], 0, v202, v202 op_sel_hi:[0,0,0]
	global_load_lds_dwordx4 v206, s[26:27]
	v_mfma_scale_f32_16x16x128_f8f6f4 v[168:171], v[132:139], v[108:115], 0, v202, v202 op_sel_hi:[0,0,0]
	v_mfma_scale_f32_16x16x128_f8f6f4 v[140:143], v[140:147], v[108:115], 0, v202, v202 op_sel_hi:[0,0,0]
	s_setprio 0
	s_add_i32 s25, 0, 0x18000
	v_add_u32_e32 v0, s25, v207
	s_barrier
	s_nop 2
	ds_read_b128 v[2:5], v0
	ds_read_b128 v[6:9], v0 offset:1024
	ds_read_b128 v[10:13], v0 offset:2048
	ds_read_b128 v[14:17], v0 offset:3072
	s_add_u32 s26, s10, 0x40000
	v_mov_b32_e32 v0, v205
	ds_read_b128 v[18:21], v208 offset:32768
	ds_read_b128 v[22:25], v208 offset:33792
	ds_read_b128 v[26:29], v208 offset:34816
	ds_read_b128 v[30:33], v208 offset:35840
	ds_read_b128 v[34:37], v208 offset:36864
	ds_read_b128 v[38:41], v208 offset:37888
	ds_read_b128 v[42:45], v208 offset:38912
	ds_read_b128 v[46:49], v208 offset:39936
	s_addc_u32 s27, s11, 0
	s_nop 0
	v_mov_b32_e32 v0, v206
	s_nop 0
	s_waitcnt lgkmcnt(8)
	s_barrier
	s_waitcnt lgkmcnt(0)
	s_setprio 1
	s_waitcnt lgkmcnt(0)
	v_mfma_scale_f32_16x16x128_f8f6f4 v[164:167], v[2:9], v[18:25], v[164:167], v202, v202 op_sel_hi:[0,0,0]
	v_mfma_scale_f32_16x16x128_f8f6f4 v[160:163], v[10:17], v[18:25], v[160:163], v202, v202 op_sel_hi:[0,0,0]
	s_mov_b32 m0, s20
	v_mfma_scale_f32_16x16x128_f8f6f4 v[156:159], v[2:9], v[26:33], v[156:159], v202, v202 op_sel_hi:[0,0,0]
	global_load_lds_dwordx4 v205, s[26:27]
	v_mfma_scale_f32_16x16x128_f8f6f4 v[152:155], v[10:17], v[26:33], v[152:155], v202, v202 op_sel_hi:[0,0,0]
	v_mfma_scale_f32_16x16x128_f8f6f4 v[148:151], v[2:9], v[34:41], v[148:151], v202, v202 op_sel_hi:[0,0,0]
	s_mov_b32 m0, s21
	v_mfma_scale_f32_16x16x128_f8f6f4 v[144:147], v[10:17], v[34:41], v[188:191], v202, v202 op_sel_hi:[0,0,0]
	global_load_lds_dwordx4 v206, s[26:27]
	v_mfma_scale_f32_16x16x128_f8f6f4 v[136:139], v[2:9], v[42:49], v[192:195], v202, v202 op_sel_hi:[0,0,0]
	v_mfma_scale_f32_16x16x128_f8f6f4 v[132:135], v[10:17], v[42:49], v[196:199], v202, v202 op_sel_hi:[0,0,0]
	s_setprio 0
	s_barrier
	s_add_i32 s26, 0, 0x1c000
	v_add_u32_e32 v0, s26, v207
	ds_read_b128 v[52:55], v0
	ds_read_b128 v[56:59], v0 offset:1024
	ds_read_b128 v[68:71], v0 offset:2048
	ds_read_b128 v[72:75], v0 offset:3072
	v_mov_b32_e32 v0, v205
	s_add_i32 s25, s25, s73
	v_lshl_add_u64 v[50:51], s[6:7], 0, v[0:1]
	v_lshl_add_u64 v[50:51], v[50:51], 0, s[66:67]
	v_mov_b32_e32 v0, v206
	v_lshl_add_u64 v[50:51], s[6:7], 0, v[0:1]
	v_lshl_add_u64 v[50:51], v[50:51], 0, s[66:67]
	s_barrier
	s_waitcnt lgkmcnt(0)
	s_setprio 1
	s_waitcnt lgkmcnt(0)
	v_mfma_scale_f32_16x16x128_f8f6f4 v[128:131], v[52:59], v[18:25], v[128:131], v202, v202 op_sel_hi:[0,0,0]
	v_mfma_scale_f32_16x16x128_f8f6f4 v[124:127], v[68:75], v[18:25], v[124:127], v202, v202 op_sel_hi:[0,0,0]
	s_add_u32 s98, s6, s66
	s_addc_u32 s99, s7, s67
	s_mov_b32 m0, s25
	v_mfma_scale_f32_16x16x128_f8f6f4 v[120:123], v[52:59], v[26:33], v[120:123], v202, v202 op_sel_hi:[0,0,0]
	global_load_lds_dwordx4 v205, s[98:99]
	v_mfma_scale_f32_16x16x128_f8f6f4 v[116:119], v[68:75], v[26:33], v[116:119], v202, v202 op_sel_hi:[0,0,0]
	v_mfma_scale_f32_16x16x128_f8f6f4 v[112:115], v[52:59], v[34:41], v[210:213], v202, v202 op_sel_hi:[0,0,0]
	s_add_i32 m0, s25, 0x2000
	v_mfma_scale_f32_16x16x128_f8f6f4 v[108:111], v[68:75], v[34:41], v[172:175], v202, v202 op_sel_hi:[0,0,0]
	global_load_lds_dwordx4 v206, s[98:99]
	v_mfma_scale_f32_16x16x128_f8f6f4 v[104:107], v[52:59], v[42:49], v[176:179], v202, v202 op_sel_hi:[0,0,0]
	v_mfma_scale_f32_16x16x128_f8f6f4 v[100:103], v[68:75], v[42:49], v[180:183], v202, v202 op_sel_hi:[0,0,0]
	s_setprio 0
	v_mov_b32_e32 v0, v205
	s_barrier
	ds_read_b128 v[18:21], v208 offset:49152
	ds_read_b128 v[22:25], v208 offset:50176
	ds_read_b128 v[84:87], v208 offset:51200
	ds_read_b128 v[88:91], v208 offset:52224
	ds_read_b128 v[92:95], v208 offset:53248
	ds_read_b128 v[96:99], v208 offset:54272
	ds_read_b128 v[172:175], v208 offset:55296
	ds_read_b128 v[176:179], v208 offset:56320
	v_lshl_add_u64 v[26:27], s[10:11], 0, v[0:1]
	v_lshl_add_u64 v[26:27], v[26:27], 0, s[66:67]
	v_mov_b32_e32 v0, v206
	v_lshl_add_u64 v[26:27], s[10:11], 0, v[0:1]
	v_lshl_add_u64 v[26:27], v[26:27], 0, s[66:67]
	s_barrier
	s_waitcnt lgkmcnt(0)
	s_setprio 1
	s_waitcnt lgkmcnt(0)
	v_mfma_scale_f32_16x16x128_f8f6f4 v[80:83], v[2:9], v[18:25], v[80:83], v202, v202 op_sel_hi:[0,0,0]
	v_mfma_scale_f32_16x16x128_f8f6f4 v[76:79], v[10:17], v[18:25], v[76:79], v202, v202 op_sel_hi:[0,0,0]
	s_add_u32 s98, s10, s66
	s_addc_u32 s99, s11, s67
	s_mov_b32 m0, s22
	v_mfma_scale_f32_16x16x128_f8f6f4 v[64:67], v[2:9], v[84:91], v[64:67], v202, v202 op_sel_hi:[0,0,0]
	global_load_lds_dwordx4 v205, s[98:99]
	v_mfma_scale_f32_16x16x128_f8f6f4 v[60:63], v[10:17], v[84:91], v[60:63], v202, v202 op_sel_hi:[0,0,0]
	v_mfma_scale_f32_16x16x128_f8f6f4 v[48:51], v[2:9], v[92:99], v[184:187], v202, v202 op_sel_hi:[0,0,0]
	s_mov_b32 m0, s34
	v_mfma_scale_f32_16x16x128_f8f6f4 v[44:47], v[10:17], v[92:99], v[214:217], v202, v202 op_sel_hi:[0,0,0]
	global_load_lds_dwordx4 v206, s[98:99]
	v_mfma_scale_f32_16x16x128_f8f6f4 v[40:43], v[2:9], v[172:179], v[218:221], v202, v202 op_sel_hi:[0,0,0]
	v_mfma_scale_f32_16x16x128_f8f6f4 v[36:39], v[10:17], v[172:179], v[222:225], v202, v202 op_sel_hi:[0,0,0]
	s_setprio 0
	s_barrier
	s_add_u32 s6, s6, 0x40080
	s_addc_u32 s7, s7, 0
	v_mov_b32_e32 v0, v205
	s_add_i32 s10, s26, s73
	s_nop 0
	v_mov_b32_e32 v0, v206
	s_nop 0
	s_waitcnt vmcnt(4)
	s_barrier
	s_setprio 1
	v_mfma_scale_f32_16x16x128_f8f6f4 v[32:35], v[52:59], v[18:25], v[226:229], v202, v202 op_sel_hi:[0,0,0]
	v_mfma_scale_f32_16x16x128_f8f6f4 v[28:31], v[68:75], v[18:25], v[230:233], v202, v202 op_sel_hi:[0,0,0]
	s_mov_b32 m0, s10
	v_mfma_scale_f32_16x16x128_f8f6f4 v[24:27], v[52:59], v[84:91], v[234:237], v202, v202 op_sel_hi:[0,0,0]
	global_load_lds_dwordx4 v205, s[6:7]
	v_mfma_scale_f32_16x16x128_f8f6f4 v[20:23], v[68:75], v[84:91], v[238:241], v202, v202 op_sel_hi:[0,0,0]
	v_mfma_scale_f32_16x16x128_f8f6f4 v[16:19], v[52:59], v[92:99], v[242:245], v202, v202 op_sel_hi:[0,0,0]
	s_add_i32 m0, s10, 0x2000
	v_mfma_scale_f32_16x16x128_f8f6f4 v[12:15], v[68:75], v[92:99], v[246:249], v202, v202 op_sel_hi:[0,0,0]
	global_load_lds_dwordx4 v206, s[6:7]
	v_mfma_scale_f32_16x16x128_f8f6f4 v[8:11], v[52:59], v[172:179], v[168:171], v202, v202 op_sel_hi:[0,0,0]
	v_mfma_scale_f32_16x16x128_f8f6f4 v[4:7], v[68:75], v[172:179], v[140:143], v202, v202 op_sel_hi:[0,0,0]
	s_setprio 0
	s_add_i32 s17, s17, 2
	s_add_u32 s4, s4, 0x100
	s_addc_u32 s5, s5, 0
	s_add_u32 s15, s15, 0x100
	s_addc_u32 s16, s16, 0
	s_cmp_gt_u32 s17, 13
	s_barrier
	s_cbranch_scc0 .LBB0_278
	s_branch .Lpeel_exit_1
	.p2align 6

.LBB0_1502:
	s_add_u32 s2, s2, 0x40080
	s_addc_u32 s3, s3, 0
	s_add_u32 s7, s34, 0x100
	v_mov_b32_e32 v0, 0
	s_addc_u32 s20, s35, 0
	s_mov_b32 s22, -2
	.p2align 6
.Lpeel_2:
	s_add_u32 s24, s2, 0xfffc0080
	s_addc_u32 s25, s3, -1
	s_add_i32 s28, 0, 0x10000
	v_add_u32_e32 v128, s28, v150
	ds_read_b128 v[136:139], v128
	ds_read_b128 v[140:143], v128 offset:1024
	ds_read_b128 v[152:155], v128 offset:2048
	ds_read_b128 v[156:159], v128 offset:3072
	s_cmp_eq_u32 s22, 12
	s_cselect_b32 s41, s49, s25
	s_cselect_b32 s40, s48, s24
	s_cselect_b32 s39, s59, s20
	s_cselect_b32 s38, s58, s7
	v_mov_b32_e32 v128, v148
	ds_read_b128 v[160:163], v151
	ds_read_b128 v[164:167], v151 offset:1024
	ds_read_b128 v[168:171], v151 offset:2048
	ds_read_b128 v[172:175], v151 offset:3072
	ds_read_b128 v[176:179], v151 offset:4096
	ds_read_b128 v[180:183], v151 offset:5120
	ds_read_b128 v[184:187], v151 offset:6144
	ds_read_b128 v[188:191], v151 offset:7168
	s_nop 0
	v_mov_b32_e32 v128, v149
	s_nop 0
	s_waitcnt lgkmcnt(8)
	s_barrier
	s_waitcnt lgkmcnt(0)
	s_setprio 1
	s_waitcnt lgkmcnt(0)
	v_mfma_scale_f32_16x16x128_f8f6f4 v[124:127], v[136:143], v[160:167], 0, v146, v146 op_sel_hi:[0,0,0]
	v_mfma_scale_f32_16x16x128_f8f6f4 v[120:123], v[152:159], v[160:167], 0, v146, v146 op_sel_hi:[0,0,0]
	s_add_i32 m0, s0, 0xc000
	v_mfma_scale_f32_16x16x128_f8f6f4 v[116:119], v[136:143], v[168:175], 0, v146, v146 op_sel_hi:[0,0,0]
	global_load_lds_dwordx4 v148, s[2:3]
	v_mfma_scale_f32_16x16x128_f8f6f4 v[112:115], v[152:159], v[168:175], 0, v146, v146 op_sel_hi:[0,0,0]
	v_mfma_scale_f32_16x16x128_f8f6f4 v[128:131], v[136:143], v[176:183], 0, v146, v146 op_sel_hi:[0,0,0]
	s_add_i32 m0, s0, 0xe000
	v_mfma_scale_f32_16x16x128_f8f6f4 v[192:195], v[152:159], v[176:183], 0, v146, v146 op_sel_hi:[0,0,0]
	global_load_lds_dwordx4 v149, s[2:3]
	v_mfma_scale_f32_16x16x128_f8f6f4 v[196:199], v[136:143], v[184:191], 0, v146, v146 op_sel_hi:[0,0,0]
	v_mfma_scale_f32_16x16x128_f8f6f4 v[200:203], v[152:159], v[184:191], 0, v146, v146 op_sel_hi:[0,0,0]
	s_setprio 0
	s_barrier
	s_add_i32 s29, 0, 0x14000
	s_nop 0
	v_add_u32_e32 v108, s29, v150
	v_mov_b32_e32 v132, v148
	s_add_i32 s24, s28, s21
	ds_read_b128 v[96:99], v108
	ds_read_b128 v[100:103], v108 offset:1024
	ds_read_b128 v[104:107], v108 offset:2048
	ds_read_b128 v[108:111], v108 offset:3072
	s_nop 0
	v_mov_b32_e32 v132, v149
	s_nop 0
	s_barrier
	s_waitcnt lgkmcnt(0)
	s_setprio 1
	s_waitcnt lgkmcnt(0)
	v_mfma_scale_f32_16x16x128_f8f6f4 v[204:207], v[96:103], v[160:167], 0, v146, v146 op_sel_hi:[0,0,0]
	v_mfma_scale_f32_16x16x128_f8f6f4 v[160:163], v[104:111], v[160:167], 0, v146, v146 op_sel_hi:[0,0,0]
	s_mov_b32 m0, s24
	v_mfma_scale_f32_16x16x128_f8f6f4 v[164:167], v[96:103], v[168:175], 0, v146, v146 op_sel_hi:[0,0,0]
	global_load_lds_dwordx4 v148, s[38:39]
	v_mfma_scale_f32_16x16x128_f8f6f4 v[168:171], v[104:111], v[168:175], 0, v146, v146 op_sel_hi:[0,0,0]
	v_mfma_scale_f32_16x16x128_f8f6f4 v[172:175], v[96:103], v[176:183], 0, v146, v146 op_sel_hi:[0,0,0]
	s_add_i32 m0, s24, 0x2000
	v_mfma_scale_f32_16x16x128_f8f6f4 v[176:179], v[104:111], v[176:183], 0, v146, v146 op_sel_hi:[0,0,0]
	global_load_lds_dwordx4 v149, s[38:39]
	v_mfma_scale_f32_16x16x128_f8f6f4 v[180:183], v[96:103], v[184:191], 0, v146, v146 op_sel_hi:[0,0,0]
	v_mfma_scale_f32_16x16x128_f8f6f4 v[184:187], v[104:111], v[184:191], 0, v146, v146 op_sel_hi:[0,0,0]
	s_setprio 0
	v_mov_b32_e32 v132, v148
	s_barrier
	s_nop 2
	ds_read_b128 v[32:35], v151 offset:16384
	ds_read_b128 v[36:39], v151 offset:17408
	ds_read_b128 v[40:43], v151 offset:18432
	ds_read_b128 v[44:47], v151 offset:19456
	ds_read_b128 v[48:51], v151 offset:20480
	ds_read_b128 v[52:55], v151 offset:21504
	ds_read_b128 v[56:59], v151 offset:22528
	ds_read_b128 v[60:63], v151 offset:23552
	s_nop 0
	v_mov_b32_e32 v132, v149
	s_nop 0
	s_barrier
	s_waitcnt lgkmcnt(0)
	s_setprio 1
	s_waitcnt lgkmcnt(0)
	v_mfma_scale_f32_16x16x128_f8f6f4 v[92:95], v[136:143], v[32:39], 0, v146, v146 op_sel_hi:[0,0,0]
	v_mfma_scale_f32_16x16x128_f8f6f4 v[88:91], v[152:159], v[32:39], 0, v146, v146 op_sel_hi:[0,0,0]
	s_mov_b32 m0, s0
	v_mfma_scale_f32_16x16x128_f8f6f4 v[84:87], v[136:143], v[40:47], 0, v146, v146 op_sel_hi:[0,0,0]
	global_load_lds_dwordx4 v148, s[40:41]
	v_mfma_scale_f32_16x16x128_f8f6f4 v[80:83], v[152:159], v[40:47], 0, v146, v146 op_sel_hi:[0,0,0]
	v_mfma_scale_f32_16x16x128_f8f6f4 v[76:79], v[136:143], v[48:55], 0, v146, v146 op_sel_hi:[0,0,0]
	s_mov_b32 m0, s1
	v_mfma_scale_f32_16x16x128_f8f6f4 v[72:75], v[152:159], v[48:55], 0, v146, v146 op_sel_hi:[0,0,0]
	global_load_lds_dwordx4 v149, s[40:41]
	v_mfma_scale_f32_16x16x128_f8f6f4 v[188:191], v[136:143], v[56:63], 0, v146, v146 op_sel_hi:[0,0,0]
	v_mfma_scale_f32_16x16x128_f8f6f4 v[208:211], v[152:159], v[56:63], 0, v146, v146 op_sel_hi:[0,0,0]
	s_setprio 0
	s_barrier
	s_add_u32 s24, s38, 0x40000
	s_addc_u32 s25, s39, 0
	s_nop 2
	v_mov_b32_e32 v64, v148
	s_add_i32 s28, s29, s21
	s_mov_b32 s100, s28
	s_nop 0
	v_mov_b32_e32 v64, v149
	s_add_i32 s101, s28, 0x2000
	s_nop 0
	s_waitcnt vmcnt(4)
	s_barrier
	s_setprio 1
	v_mfma_scale_f32_16x16x128_f8f6f4 v[212:215], v[96:103], v[32:39], 0, v146, v146 op_sel_hi:[0,0,0]
	v_mfma_scale_f32_16x16x128_f8f6f4 v[216:219], v[104:111], v[32:39], 0, v146, v146 op_sel_hi:[0,0,0]
	s_mov_b32 m0, s100
	v_mfma_scale_f32_16x16x128_f8f6f4 v[220:223], v[96:103], v[40:47], 0, v146, v146 op_sel_hi:[0,0,0]
	global_load_lds_dwordx4 v148, s[24:25]
	v_mfma_scale_f32_16x16x128_f8f6f4 v[224:227], v[104:111], v[40:47], 0, v146, v146 op_sel_hi:[0,0,0]
	v_mfma_scale_f32_16x16x128_f8f6f4 v[228:231], v[96:103], v[48:55], 0, v146, v146 op_sel_hi:[0,0,0]
	s_mov_b32 m0, s101
	v_mfma_scale_f32_16x16x128_f8f6f4 v[232:235], v[104:111], v[48:55], 0, v146, v146 op_sel_hi:[0,0,0]
	global_load_lds_dwordx4 v149, s[24:25]
	v_mfma_scale_f32_16x16x128_f8f6f4 v[236:239], v[96:103], v[56:63], 0, v146, v146 op_sel_hi:[0,0,0]
	v_mfma_scale_f32_16x16x128_f8f6f4 v[240:243], v[104:111], v[56:63], 0, v146, v146 op_sel_hi:[0,0,0]
	s_setprio 0
	s_add_i32 s28, 0, 0x18000
	s_nop 1
	v_add_u32_e32 v12, s28, v150
	s_barrier
	s_nop 0
	ds_read_b128 v[0:3], v12
	ds_read_b128 v[4:7], v12 offset:1024
	ds_read_b128 v[8:11], v12 offset:2048
	ds_read_b128 v[12:15], v12 offset:3072
	s_add_u32 s24, s40, 0x40000
	v_mov_b32_e32 v40, v148
	ds_read_b128 v[16:19], v151 offset:32768
	ds_read_b128 v[20:23], v151 offset:33792
	ds_read_b128 v[24:27], v151 offset:34816
	ds_read_b128 v[28:31], v151 offset:35840
	ds_read_b128 v[32:35], v151 offset:36864
	ds_read_b128 v[36:39], v151 offset:37888
	ds_read_b128 v[64:67], v151 offset:38912
	ds_read_b128 v[68:71], v151 offset:39936
	s_addc_u32 s25, s41, 0
	s_nop 0
	v_mov_b32_e32 v40, v149
	s_nop 0
	s_waitcnt lgkmcnt(8)
	s_barrier
	s_waitcnt lgkmcnt(0)
	s_setprio 1
	s_waitcnt lgkmcnt(0)
	v_mfma_scale_f32_16x16x128_f8f6f4 v[124:127], v[0:7], v[16:23], v[124:127], v146, v146 op_sel_hi:[0,0,0]
	v_mfma_scale_f32_16x16x128_f8f6f4 v[120:123], v[8:15], v[16:23], v[120:123], v146, v146 op_sel_hi:[0,0,0]
	s_mov_b32 m0, s8
	v_mfma_scale_f32_16x16x128_f8f6f4 v[116:119], v[0:7], v[24:31], v[116:119], v146, v146 op_sel_hi:[0,0,0]
	global_load_lds_dwordx4 v148, s[24:25]
	v_mfma_scale_f32_16x16x128_f8f6f4 v[112:115], v[8:15], v[24:31], v[112:115], v146, v146 op_sel_hi:[0,0,0]
	v_mfma_scale_f32_16x16x128_f8f6f4 v[108:111], v[0:7], v[32:39], v[128:131], v146, v146 op_sel_hi:[0,0,0]
	s_mov_b32 m0, s9
	v_mfma_scale_f32_16x16x128_f8f6f4 v[104:107], v[8:15], v[32:39], v[192:195], v146, v146 op_sel_hi:[0,0,0]
	global_load_lds_dwordx4 v149, s[24:25]
	v_mfma_scale_f32_16x16x128_f8f6f4 v[100:103], v[0:7], v[64:71], v[196:199], v146, v146 op_sel_hi:[0,0,0]
	v_mfma_scale_f32_16x16x128_f8f6f4 v[96:99], v[8:15], v[64:71], v[200:203], v146, v146 op_sel_hi:[0,0,0]
	s_setprio 0
	s_barrier
	s_add_i32 s29, 0, 0x1c000
	v_add_u32_e32 v40, s29, v150
	v_mov_b32_e32 v132, v148
	ds_read_b128 v[136:139], v40
	ds_read_b128 v[140:143], v40 offset:1024
	ds_read_b128 v[152:155], v40 offset:2048
	ds_read_b128 v[156:159], v40 offset:3072
	s_add_i32 s24, s28, s21
	v_lshl_add_u64 v[40:41], s[38:39], 0, v[132:133]
	v_lshl_add_u64 v[40:41], v[40:41], 0, s[52:53]
	v_mov_b32_e32 v132, v149
	v_lshl_add_u64 v[40:41], s[38:39], 0, v[132:133]
	v_lshl_add_u64 v[40:41], v[40:41], 0, s[52:53]
	s_barrier
	s_waitcnt lgkmcnt(0)
	s_setprio 1
	s_waitcnt lgkmcnt(0)
	v_mfma_scale_f32_16x16x128_f8f6f4 v[60:63], v[136:143], v[16:23], v[204:207], v146, v146 op_sel_hi:[0,0,0]
	v_mfma_scale_f32_16x16x128_f8f6f4 v[56:59], v[152:159], v[16:23], v[160:163], v146, v146 op_sel_hi:[0,0,0]
	s_add_u32 s98, s38, s52
	s_addc_u32 s99, s39, s53
	s_mov_b32 m0, s24
	v_mfma_scale_f32_16x16x128_f8f6f4 v[52:55], v[136:143], v[24:31], v[164:167], v146, v146 op_sel_hi:[0,0,0]
	global_load_lds_dwordx4 v148, s[98:99]
	v_mfma_scale_f32_16x16x128_f8f6f4 v[48:51], v[152:159], v[24:31], v[168:171], v146, v146 op_sel_hi:[0,0,0]
	v_mfma_scale_f32_16x16x128_f8f6f4 v[44:47], v[136:143], v[32:39], v[172:175], v146, v146 op_sel_hi:[0,0,0]
	s_add_i32 m0, s24, 0x2000
	v_mfma_scale_f32_16x16x128_f8f6f4 v[40:43], v[152:159], v[32:39], v[176:179], v146, v146 op_sel_hi:[0,0,0]
	global_load_lds_dwordx4 v149, s[98:99]
	v_mfma_scale_f32_16x16x128_f8f6f4 v[36:39], v[136:143], v[64:71], v[180:183], v146, v146 op_sel_hi:[0,0,0]
	v_mfma_scale_f32_16x16x128_f8f6f4 v[32:35], v[152:159], v[64:71], v[184:187], v146, v146 op_sel_hi:[0,0,0]
	s_setprio 0
	v_mov_b32_e32 v132, v148
	s_barrier
	ds_read_b128 v[16:19], v151 offset:49152
	ds_read_b128 v[20:23], v151 offset:50176
	ds_read_b128 v[160:163], v151 offset:51200
	ds_read_b128 v[164:167], v151 offset:52224
	ds_read_b128 v[168:171], v151 offset:53248
	ds_read_b128 v[172:175], v151 offset:54272
	ds_read_b128 v[176:179], v151 offset:55296
	ds_read_b128 v[180:183], v151 offset:56320
	v_lshl_add_u64 v[24:25], s[40:41], 0, v[132:133]
	v_lshl_add_u64 v[24:25], v[24:25], 0, s[52:53]
	v_mov_b32_e32 v132, v149
	v_lshl_add_u64 v[24:25], s[40:41], 0, v[132:133]
	v_lshl_add_u64 v[24:25], v[24:25], 0, s[52:53]
	s_barrier
	s_waitcnt lgkmcnt(0)
	s_setprio 1
	s_waitcnt lgkmcnt(0)
	v_mfma_scale_f32_16x16x128_f8f6f4 v[92:95], v[0:7], v[16:23], v[92:95], v146, v146 op_sel_hi:[0,0,0]
	v_mfma_scale_f32_16x16x128_f8f6f4 v[88:91], v[8:15], v[16:23], v[88:91], v146, v146 op_sel_hi:[0,0,0]
	s_add_u32 s98, s40, s52
	s_addc_u32 s99, s41, s53
	s_mov_b32 m0, s10
	v_mfma_scale_f32_16x16x128_f8f6f4 v[84:87], v[0:7], v[160:167], v[84:87], v146, v146 op_sel_hi:[0,0,0]
	global_load_lds_dwordx4 v148, s[98:99]
	v_mfma_scale_f32_16x16x128_f8f6f4 v[80:83], v[8:15], v[160:167], v[80:83], v146, v146 op_sel_hi:[0,0,0]
	v_mfma_scale_f32_16x16x128_f8f6f4 v[76:79], v[0:7], v[168:175], v[76:79], v146, v146 op_sel_hi:[0,0,0]
	s_mov_b32 m0, s11
	v_mfma_scale_f32_16x16x128_f8f6f4 v[72:75], v[8:15], v[168:175], v[72:75], v146, v146 op_sel_hi:[0,0,0]
	global_load_lds_dwordx4 v149, s[98:99]
	v_mfma_scale_f32_16x16x128_f8f6f4 v[68:71], v[0:7], v[176:183], v[188:191], v146, v146 op_sel_hi:[0,0,0]
	v_mfma_scale_f32_16x16x128_f8f6f4 v[64:67], v[8:15], v[176:183], v[208:211], v146, v146 op_sel_hi:[0,0,0]
	s_setprio 0
	s_barrier
	s_add_u32 s24, s38, 0x40080
	s_addc_u32 s25, s39, 0
	v_mov_b32_e32 v0, v148
	s_add_i32 s28, s29, s21
	s_nop 0
	v_mov_b32_e32 v0, v149
	s_nop 0
	s_waitcnt vmcnt(4)
	s_barrier
	s_setprio 1
	v_mfma_scale_f32_16x16x128_f8f6f4 v[28:31], v[136:143], v[16:23], v[212:215], v146, v146 op_sel_hi:[0,0,0]
	v_mfma_scale_f32_16x16x128_f8f6f4 v[24:27], v[152:159], v[16:23], v[216:219], v146, v146 op_sel_hi:[0,0,0]
	s_mov_b32 m0, s28
	v_mfma_scale_f32_16x16x128_f8f6f4 v[20:23], v[136:143], v[160:167], v[220:223], v146, v146 op_sel_hi:[0,0,0]
	global_load_lds_dwordx4 v148, s[24:25]
	v_mfma_scale_f32_16x16x128_f8f6f4 v[16:19], v[152:159], v[160:167], v[224:227], v146, v146 op_sel_hi:[0,0,0]
	v_mfma_scale_f32_16x16x128_f8f6f4 v[12:15], v[136:143], v[168:175], v[228:231], v146, v146 op_sel_hi:[0,0,0]
	s_add_i32 m0, s28, 0x2000
	v_mfma_scale_f32_16x16x128_f8f6f4 v[8:11], v[152:159], v[168:175], v[232:235], v146, v146 op_sel_hi:[0,0,0]
	global_load_lds_dwordx4 v149, s[24:25]
	v_mfma_scale_f32_16x16x128_f8f6f4 v[4:7], v[136:143], v[176:183], v[236:239], v146, v146 op_sel_hi:[0,0,0]
	v_mfma_scale_f32_16x16x128_f8f6f4 v[0:3], v[152:159], v[176:183], v[240:243], v146, v146 op_sel_hi:[0,0,0]
	s_setprio 0
	s_add_i32 s22, s22, 2
	s_add_u32 s2, s2, 0x100
	s_addc_u32 s3, s3, 0
	s_add_u32 s7, s7, 0x100
	s_addc_u32 s20, s20, 0
	s_cmp_gt_u32 s22, 13
	s_barrier
	s_cbranch_scc0 .LBB0_1503
	s_branch .Lpeel_exit_2
	.p2align 6

.LBB0_1935:
	s_add_u32 s48, s14, 0x2f1c8000
	v_readlane_b32 s8, v252, 10
	v_mov_b32_e32 v178, v181
	v_mov_b32_e32 v179, 0
	s_addc_u32 s49, s15, 0
	s_lshl_b32 s8, s8, 5
	s_waitcnt vmcnt(4)
	s_barrier
	s_mov_b64 s[12:13], 0x80
	v_lshl_add_u64 v[4:5], s[36:37], 0, v[178:179]
	s_and_b32 s51, s8, 0x60
	s_add_i32 m0, s31, 0x18000
	v_lshl_add_u64 v[4:5], v[4:5], 0, s[12:13]
	v_mov_b32_e32 v178, v183
	s_lshl_b32 s50, s5, 6
	s_lshl_b32 s5, s5, 13
	s_lshr_b32 s8, s51, 3
	global_load_lds_dwordx4 v[4:5], off
	s_add_i32 m0, s31, 0x1a000
	v_lshl_add_u64 v[4:5], s[36:37], 0, v[178:179]
	v_lshl_add_u64 v[4:5], v[4:5], 0, s[12:13]
	s_add_u32 s14, s14, 0x249c8080
	global_load_lds_dwordx4 v[4:5], off
	s_addc_u32 s15, s15, 0
	v_mov_b32_e32 v4, v184
	s_add_i32 s52, s31, 0x8000
	s_mov_b32 m0, s52
	s_add_i32 s53, s31, 0xa000
	global_load_lds_dwordx4 v4, s[14:15]
	v_mov_b32_e32 v4, v185
	s_mov_b32 m0, s53
	v_readlane_b32 s18, v252, 3
	global_load_lds_dwordx4 v4, s[14:15]
	s_add_u32 s14, s36, 0x40080
	v_mov_b32_e32 v4, v181
	s_addc_u32 s15, s37, 0
	s_add_i32 m0, s31, 0x1c000
	v_readlane_b32 s19, v252, 4
	global_load_lds_dwordx4 v4, s[14:15]
	v_mov_b32_e32 v4, v183
	s_add_i32 m0, s31, 0x1e000
	v_and_b32_e32 v5, 48, v176
	global_load_lds_dwordx4 v4, s[14:15]
	v_ashrrev_i32_e32 v4, 6, v176
	v_lshl_add_u32 v6, v4, 10, s5
	v_lshlrev_b32_e32 v7, 6, v176
	s_movk_i32 s5, 0x3c0
	s_load_dwordx2 s[18:19], s[18:19], 0xb8
	v_and_or_b32 v5, v7, s5, v5
	v_readlane_b32 s5, v252, 2
	s_cmpk_lt_u32 s5, 0x100
	v_add_lshl_u32 v4, v4, s8, 10
	s_cselect_b64 s[14:15], -1, 0
	s_lshl_b32 s5, s4, 2
	s_add_i32 s8, 0, 0x21000
	v_lshlrev_b32_e32 v1, 2, v1
	v_lshlrev_b32_e32 v0, 2, v0
	v_lshlrev_b32_e32 v3, 2, v3
	v_lshlrev_b32_e32 v2, 2, v2
	v_lshlrev_b32_e32 v7, 2, v176
	s_add_i32 s54, s8, s5
	s_ashr_i32 s5, s4, 31
	v_add3_u32 v189, s8, v1, v0
	v_add3_u32 v190, s8, v3, v2
	s_add_i32 s8, 0, 0x21200
	v_and_b32_e32 v7, 32, v7
	v_add3_u32 v191, s8, v1, v0
	v_add3_u32 v192, s8, v3, v2
	s_waitcnt lgkmcnt(0)
	s_add_u32 s8, s18, s16
	v_bitop3_b32 v188, v5, v4, v7 bitop3:0xde
	s_waitcnt vmcnt(6)
	s_addc_u32 s17, s19, s17
	v_bitop3_b32 v6, v5, v6, v7 bitop3:0xde
	s_add_u32 s16, s8, 0x249c8080
	v_add_u32_e32 v0, 0, v188
	v_ashrrev_i32_e32 v177, 31, v176
	s_addc_u32 s17, s17, 0
	s_add_i32 s55, 0, 0x20104
	s_lshl_b64 s[18:19], s[4:5], 2
	v_add_u32_e32 v193, 0x10000, v0
	v_add_u32_e32 v194, 0, v6
	v_mov_b32_e32 v195, 0x7f7f7f7f
	s_add_i32 s5, 0, 0x14000
	s_movk_i32 s56, 0x600
	s_mov_b32 s20, 0x3c800000
	s_mov_b32 s57, 0
	s_mov_b64 s[26:27], s[36:37]
	s_barrier
	s_branch .LBB0_1937
	.p2align 6

.LBB0_2381:
	s_add_u32 s16, s16, 0x30080
	s_addc_u32 s17, s17, 0
	s_add_u32 s52, s18, 0x100
	v_mov_b32_e32 v0, 0
	s_addc_u32 s53, s19, 0
	s_mov_b32 s54, -2
	.p2align 6
.Lpeel_4:
	ds_read_b128 v[140:143], v134
	ds_read_b128 v[144:147], v134 offset:1024
	ds_read_b128 v[148:151], v134 offset:2048
	ds_read_b128 v[152:155], v134 offset:3072
	s_add_u32 s18, s16, 0xfffd0080
	s_addc_u32 s19, s17, -1
	s_cmp_eq_u32 s54, 8
	s_cselect_b32 s21, s15, s19
	s_cselect_b32 s20, s14, s18
	s_cselect_b32 s19, s13, s53
	s_cselect_b32 s18, s12, s52
	v_mov_b32_e32 v128, v132
	ds_read_b128 v[156:159], v135
	ds_read_b128 v[160:163], v135 offset:1024
	ds_read_b128 v[164:167], v135 offset:2048
	ds_read_b128 v[168:171], v135 offset:3072
	ds_read_b128 v[172:175], v135 offset:4096
	ds_read_b128 v[176:179], v135 offset:5120
	ds_read_b128 v[180:183], v135 offset:6144
	ds_read_b128 v[184:187], v135 offset:7168
	s_nop 0
	v_mov_b32_e32 v128, v133
	s_nop 0
	s_waitcnt lgkmcnt(8)
	s_barrier
	s_waitcnt lgkmcnt(0)
	s_setprio 1
	s_waitcnt lgkmcnt(0)
	v_mfma_scale_f32_16x16x128_f8f6f4 v[124:127], v[140:147], v[156:163], 0, v136, v136 op_sel_hi:[0,0,0]
	v_mfma_scale_f32_16x16x128_f8f6f4 v[120:123], v[148:155], v[156:163], 0, v136, v136 op_sel_hi:[0,0,0]
	s_mov_b32 m0, s39
	v_mfma_scale_f32_16x16x128_f8f6f4 v[116:119], v[140:147], v[164:171], 0, v136, v136 op_sel_hi:[0,0,0]
	global_load_lds_dwordx4 v132, s[16:17]
	v_mfma_scale_f32_16x16x128_f8f6f4 v[112:115], v[148:155], v[164:171], 0, v136, v136 op_sel_hi:[0,0,0]
	v_mfma_scale_f32_16x16x128_f8f6f4 v[188:191], v[140:147], v[172:179], 0, v136, v136 op_sel_hi:[0,0,0]
	s_mov_b32 m0, s40
	v_mfma_scale_f32_16x16x128_f8f6f4 v[192:195], v[148:155], v[172:179], 0, v136, v136 op_sel_hi:[0,0,0]
	global_load_lds_dwordx4 v133, s[16:17]
	v_mfma_scale_f32_16x16x128_f8f6f4 v[196:199], v[140:147], v[180:187], 0, v136, v136 op_sel_hi:[0,0,0]
	v_mfma_scale_f32_16x16x128_f8f6f4 v[200:203], v[148:155], v[180:187], 0, v136, v136 op_sel_hi:[0,0,0]
	s_setprio 0
	s_barrier
	v_mov_b32_e32 v128, v132
	s_nop 2
	ds_read_b128 v[96:99], v137
	ds_read_b128 v[100:103], v137 offset:1024
	ds_read_b128 v[104:107], v137 offset:2048
	ds_read_b128 v[108:111], v137 offset:3072
	s_nop 0
	v_mov_b32_e32 v128, v133
	s_nop 0
	s_barrier
	s_waitcnt lgkmcnt(0)
	s_setprio 1
	s_waitcnt lgkmcnt(0)
	v_mfma_scale_f32_16x16x128_f8f6f4 v[204:207], v[96:103], v[156:163], 0, v136, v136 op_sel_hi:[0,0,0]
	v_mfma_scale_f32_16x16x128_f8f6f4 v[156:159], v[104:111], v[156:163], 0, v136, v136 op_sel_hi:[0,0,0]
	s_mov_b32 m0, s41
	v_mfma_scale_f32_16x16x128_f8f6f4 v[160:163], v[96:103], v[164:171], 0, v136, v136 op_sel_hi:[0,0,0]
	global_load_lds_dwordx4 v132, s[18:19]
	v_mfma_scale_f32_16x16x128_f8f6f4 v[164:167], v[104:111], v[164:171], 0, v136, v136 op_sel_hi:[0,0,0]
	v_mfma_scale_f32_16x16x128_f8f6f4 v[168:171], v[96:103], v[172:179], 0, v136, v136 op_sel_hi:[0,0,0]
	s_mov_b32 m0, s42
	v_mfma_scale_f32_16x16x128_f8f6f4 v[172:175], v[104:111], v[172:179], 0, v136, v136 op_sel_hi:[0,0,0]
	global_load_lds_dwordx4 v133, s[18:19]
	v_mfma_scale_f32_16x16x128_f8f6f4 v[176:179], v[96:103], v[180:187], 0, v136, v136 op_sel_hi:[0,0,0]
	v_mfma_scale_f32_16x16x128_f8f6f4 v[180:183], v[104:111], v[180:187], 0, v136, v136 op_sel_hi:[0,0,0]
	s_setprio 0
	v_mov_b32_e32 v128, v132
	s_barrier
	s_nop 2
	ds_read_b128 v[64:67], v135 offset:16384
	ds_read_b128 v[68:71], v135 offset:17408
	ds_read_b128 v[72:75], v135 offset:18432
	ds_read_b128 v[76:79], v135 offset:19456
	ds_read_b128 v[80:83], v135 offset:20480
	ds_read_b128 v[84:87], v135 offset:21504
	ds_read_b128 v[88:91], v135 offset:22528
	ds_read_b128 v[92:95], v135 offset:23552
	s_nop 0
	v_mov_b32_e32 v128, v133
	s_nop 0
	s_barrier
	s_waitcnt lgkmcnt(0)
	s_setprio 1
	s_waitcnt lgkmcnt(0)
	v_mfma_scale_f32_16x16x128_f8f6f4 v[60:63], v[140:147], v[64:71], 0, v136, v136 op_sel_hi:[0,0,0]
	v_mfma_scale_f32_16x16x128_f8f6f4 v[56:59], v[148:155], v[64:71], 0, v136, v136 op_sel_hi:[0,0,0]
	s_mov_b32 m0, s25
	v_mfma_scale_f32_16x16x128_f8f6f4 v[52:55], v[140:147], v[72:79], 0, v136, v136 op_sel_hi:[0,0,0]
	global_load_lds_dwordx4 v132, s[20:21]
	v_mfma_scale_f32_16x16x128_f8f6f4 v[48:51], v[148:155], v[72:79], 0, v136, v136 op_sel_hi:[0,0,0]
	v_mfma_scale_f32_16x16x128_f8f6f4 v[184:187], v[140:147], v[80:87], 0, v136, v136 op_sel_hi:[0,0,0]
	s_mov_b32 m0, s26
	v_mfma_scale_f32_16x16x128_f8f6f4 v[208:211], v[148:155], v[80:87], 0, v136, v136 op_sel_hi:[0,0,0]
	global_load_lds_dwordx4 v133, s[20:21]
	v_mfma_scale_f32_16x16x128_f8f6f4 v[212:215], v[140:147], v[88:95], 0, v136, v136 op_sel_hi:[0,0,0]
	v_mfma_scale_f32_16x16x128_f8f6f4 v[216:219], v[148:155], v[88:95], 0, v136, v136 op_sel_hi:[0,0,0]
	s_setprio 0
	s_barrier
	s_add_u32 s56, s18, 0x30000
	s_nop 3
	v_mov_b32_e32 v32, v132
	s_addc_u32 s57, s19, 0
	s_nop 0
	v_mov_b32_e32 v32, v133
	s_nop 0
	s_waitcnt vmcnt(4)
	s_barrier
	s_setprio 1
	v_mfma_scale_f32_16x16x128_f8f6f4 v[220:223], v[96:103], v[64:71], 0, v136, v136 op_sel_hi:[0,0,0]
	v_mfma_scale_f32_16x16x128_f8f6f4 v[224:227], v[104:111], v[64:71], 0, v136, v136 op_sel_hi:[0,0,0]
	s_mov_b32 m0, s43
	v_mfma_scale_f32_16x16x128_f8f6f4 v[228:231], v[96:103], v[72:79], 0, v136, v136 op_sel_hi:[0,0,0]
	global_load_lds_dwordx4 v132, s[56:57]
	v_mfma_scale_f32_16x16x128_f8f6f4 v[232:235], v[104:111], v[72:79], 0, v136, v136 op_sel_hi:[0,0,0]
	v_mfma_scale_f32_16x16x128_f8f6f4 v[236:239], v[96:103], v[80:87], 0, v136, v136 op_sel_hi:[0,0,0]
	s_mov_b32 m0, s44
	v_mfma_scale_f32_16x16x128_f8f6f4 v[240:243], v[104:111], v[80:87], 0, v136, v136 op_sel_hi:[0,0,0]
	global_load_lds_dwordx4 v133, s[56:57]
	v_mfma_scale_f32_16x16x128_f8f6f4 v[244:247], v[96:103], v[88:95], 0, v136, v136 op_sel_hi:[0,0,0]
	v_mfma_scale_f32_16x16x128_f8f6f4 v[248:251], v[104:111], v[88:95], 0, v136, v136 op_sel_hi:[0,0,0]
	s_setprio 0
	s_barrier
	s_nop 4
	ds_read_b128 v[0:3], v138
	ds_read_b128 v[4:7], v138 offset:1024
	ds_read_b128 v[8:11], v138 offset:2048
	ds_read_b128 v[12:15], v138 offset:3072
	s_add_u32 s56, s20, 0x30000
	v_mov_b32_e32 v64, v132
	ds_read_b128 v[16:19], v135 offset:32768
	ds_read_b128 v[20:23], v135 offset:33792
	ds_read_b128 v[24:27], v135 offset:34816
	ds_read_b128 v[28:31], v135 offset:35840
	ds_read_b128 v[32:35], v135 offset:36864
	ds_read_b128 v[36:39], v135 offset:37888
	ds_read_b128 v[40:43], v135 offset:38912
	ds_read_b128 v[44:47], v135 offset:39936
	s_addc_u32 s57, s21, 0
	s_nop 0
	v_mov_b32_e32 v64, v133
	s_nop 0
	s_waitcnt lgkmcnt(8)
	s_barrier
	s_waitcnt lgkmcnt(0)
	s_setprio 1
	s_waitcnt lgkmcnt(0)
	v_mfma_scale_f32_16x16x128_f8f6f4 v[124:127], v[0:7], v[16:23], v[124:127], v136, v136 op_sel_hi:[0,0,0]
	v_mfma_scale_f32_16x16x128_f8f6f4 v[120:123], v[8:15], v[16:23], v[120:123], v136, v136 op_sel_hi:[0,0,0]
	s_mov_b32 m0, s27
	v_mfma_scale_f32_16x16x128_f8f6f4 v[116:119], v[0:7], v[24:31], v[116:119], v136, v136 op_sel_hi:[0,0,0]
	global_load_lds_dwordx4 v132, s[56:57]
	v_mfma_scale_f32_16x16x128_f8f6f4 v[112:115], v[8:15], v[24:31], v[112:115], v136, v136 op_sel_hi:[0,0,0]
	v_mfma_scale_f32_16x16x128_f8f6f4 v[108:111], v[0:7], v[32:39], v[188:191], v136, v136 op_sel_hi:[0,0,0]
	s_mov_b32 m0, s28
	v_mfma_scale_f32_16x16x128_f8f6f4 v[104:107], v[8:15], v[32:39], v[192:195], v136, v136 op_sel_hi:[0,0,0]
	global_load_lds_dwordx4 v133, s[56:57]
	v_mfma_scale_f32_16x16x128_f8f6f4 v[100:103], v[0:7], v[40:47], v[196:199], v136, v136 op_sel_hi:[0,0,0]
	v_mfma_scale_f32_16x16x128_f8f6f4 v[96:99], v[8:15], v[40:47], v[200:203], v136, v136 op_sel_hi:[0,0,0]
	s_setprio 0
	s_barrier
	v_mov_b32_e32 v128, v132
	ds_read_b128 v[140:143], v139
	ds_read_b128 v[144:147], v139 offset:1024
	ds_read_b128 v[148:151], v139 offset:2048
	ds_read_b128 v[152:155], v139 offset:3072
	v_lshl_add_u64 v[64:65], s[18:19], 0, v[128:129]
	v_lshl_add_u64 v[64:65], v[64:65], 0, s[4:5]
	v_mov_b32_e32 v128, v133
	v_lshl_add_u64 v[64:65], s[18:19], 0, v[128:129]
	v_lshl_add_u64 v[64:65], v[64:65], 0, s[4:5]
	s_barrier
	s_waitcnt lgkmcnt(0)
	s_setprio 1
	s_waitcnt lgkmcnt(0)
	v_mfma_scale_f32_16x16x128_f8f6f4 v[92:95], v[140:147], v[16:23], v[204:207], v136, v136 op_sel_hi:[0,0,0]
	v_mfma_scale_f32_16x16x128_f8f6f4 v[88:91], v[148:155], v[16:23], v[156:159], v136, v136 op_sel_hi:[0,0,0]
	s_add_u32 s98, s18, s4
	s_addc_u32 s99, s19, s5
	s_mov_b32 m0, s46
	v_mfma_scale_f32_16x16x128_f8f6f4 v[84:87], v[140:147], v[24:31], v[160:163], v136, v136 op_sel_hi:[0,0,0]
	global_load_lds_dwordx4 v132, s[98:99]
	v_mfma_scale_f32_16x16x128_f8f6f4 v[80:83], v[148:155], v[24:31], v[164:167], v136, v136 op_sel_hi:[0,0,0]
	v_mfma_scale_f32_16x16x128_f8f6f4 v[76:79], v[140:147], v[32:39], v[168:171], v136, v136 op_sel_hi:[0,0,0]
	s_mov_b32 m0, s47
	v_mfma_scale_f32_16x16x128_f8f6f4 v[72:75], v[148:155], v[32:39], v[172:175], v136, v136 op_sel_hi:[0,0,0]
	global_load_lds_dwordx4 v133, s[98:99]
	v_mfma_scale_f32_16x16x128_f8f6f4 v[68:71], v[140:147], v[40:47], v[176:179], v136, v136 op_sel_hi:[0,0,0]
	v_mfma_scale_f32_16x16x128_f8f6f4 v[64:67], v[148:155], v[40:47], v[180:183], v136, v136 op_sel_hi:[0,0,0]
	s_setprio 0
	v_mov_b32_e32 v128, v132
	s_barrier
	ds_read_b128 v[16:19], v135 offset:49152
	ds_read_b128 v[20:23], v135 offset:50176
	ds_read_b128 v[156:159], v135 offset:51200
	ds_read_b128 v[160:163], v135 offset:52224
	ds_read_b128 v[164:167], v135 offset:53248
	ds_read_b128 v[168:171], v135 offset:54272
	ds_read_b128 v[172:175], v135 offset:55296
	ds_read_b128 v[176:179], v135 offset:56320
	v_lshl_add_u64 v[24:25], s[20:21], 0, v[128:129]
	v_lshl_add_u64 v[24:25], v[24:25], 0, s[4:5]
	v_mov_b32_e32 v128, v133
	v_lshl_add_u64 v[24:25], s[20:21], 0, v[128:129]
	v_lshl_add_u64 v[24:25], v[24:25], 0, s[4:5]
	s_barrier
	s_waitcnt lgkmcnt(0)
	s_setprio 1
	s_waitcnt lgkmcnt(0)
	v_mfma_scale_f32_16x16x128_f8f6f4 v[60:63], v[0:7], v[16:23], v[60:63], v136, v136 op_sel_hi:[0,0,0]
	v_mfma_scale_f32_16x16x128_f8f6f4 v[56:59], v[8:15], v[16:23], v[56:59], v136, v136 op_sel_hi:[0,0,0]
	s_add_u32 s98, s20, s4
	s_addc_u32 s99, s21, s5
	s_mov_b32 m0, s36
	v_mfma_scale_f32_16x16x128_f8f6f4 v[52:55], v[0:7], v[156:163], v[52:55], v136, v136 op_sel_hi:[0,0,0]
	global_load_lds_dwordx4 v132, s[98:99]
	v_mfma_scale_f32_16x16x128_f8f6f4 v[48:51], v[8:15], v[156:163], v[48:51], v136, v136 op_sel_hi:[0,0,0]
	v_mfma_scale_f32_16x16x128_f8f6f4 v[44:47], v[0:7], v[164:171], v[184:187], v136, v136 op_sel_hi:[0,0,0]
	s_mov_b32 m0, s37
	v_mfma_scale_f32_16x16x128_f8f6f4 v[40:43], v[8:15], v[164:171], v[208:211], v136, v136 op_sel_hi:[0,0,0]
	global_load_lds_dwordx4 v133, s[98:99]
	v_mfma_scale_f32_16x16x128_f8f6f4 v[36:39], v[0:7], v[172:179], v[212:215], v136, v136 op_sel_hi:[0,0,0]
	v_mfma_scale_f32_16x16x128_f8f6f4 v[32:35], v[8:15], v[172:179], v[216:219], v136, v136 op_sel_hi:[0,0,0]
	s_setprio 0
	s_barrier
	s_add_u32 s18, s18, 0x30080
	s_addc_u32 s19, s19, 0
	v_mov_b32_e32 v0, v132
	s_add_i32 s20, s45, s24
	s_nop 0
	v_mov_b32_e32 v0, v133
	s_nop 0
	s_waitcnt vmcnt(4)
	s_barrier
	s_setprio 1
	v_mfma_scale_f32_16x16x128_f8f6f4 v[28:31], v[140:147], v[16:23], v[220:223], v136, v136 op_sel_hi:[0,0,0]
	v_mfma_scale_f32_16x16x128_f8f6f4 v[24:27], v[148:155], v[16:23], v[224:227], v136, v136 op_sel_hi:[0,0,0]
	s_mov_b32 m0, s20
	v_mfma_scale_f32_16x16x128_f8f6f4 v[20:23], v[140:147], v[156:163], v[228:231], v136, v136 op_sel_hi:[0,0,0]
	global_load_lds_dwordx4 v132, s[18:19]
	v_mfma_scale_f32_16x16x128_f8f6f4 v[16:19], v[148:155], v[156:163], v[232:235], v136, v136 op_sel_hi:[0,0,0]
	v_mfma_scale_f32_16x16x128_f8f6f4 v[12:15], v[140:147], v[164:171], v[236:239], v136, v136 op_sel_hi:[0,0,0]
	s_add_i32 m0, s20, 0x2000
	v_mfma_scale_f32_16x16x128_f8f6f4 v[8:11], v[148:155], v[164:171], v[240:243], v136, v136 op_sel_hi:[0,0,0]
	global_load_lds_dwordx4 v133, s[18:19]
	v_mfma_scale_f32_16x16x128_f8f6f4 v[4:7], v[140:147], v[172:179], v[244:247], v136, v136 op_sel_hi:[0,0,0]
	v_mfma_scale_f32_16x16x128_f8f6f4 v[0:3], v[148:155], v[172:179], v[248:251], v136, v136 op_sel_hi:[0,0,0]
	s_setprio 0
	s_add_i32 s54, s54, 2
	s_add_u32 s16, s16, 0x100
	s_addc_u32 s17, s17, 0
	s_add_u32 s52, s52, 0x100
	s_addc_u32 s53, s53, 0
	s_cmp_gt_u32 s54, 9
	s_barrier
	s_cbranch_scc0 .LBB0_2382
	s_branch .Lpeel_exit_4
	.p2align 6

.LBB0_3993:
	v_mbcnt_lo_u32_b32 v2, -1, 0
	v_mbcnt_hi_u32_b32 v2, -1, v2
	s_lshl_b32 s22, s10, 8
	v_add_u32_e32 v0, s58, v2
	v_ashrrev_i32_e32 v0, 1, v0
	v_add_u32_e32 v0, s22, v0
	v_ashrrev_i32_e32 v1, 31, v0
	v_readlane_b32 s8, v253, 54
	v_lshlrev_b64 v[0:1], 6, v[0:1]
	v_readlane_b32 s9, v253, 55
	v_lshlrev_b32_e32 v2, 4, v2
	v_and_b32_e32 v170, 16, v2
	v_lshl_add_u64 v[0:1], s[8:9], 0, v[0:1]
	s_lshl_b32 s8, s23, 3
	s_ashr_i32 s9, s8, 31
	v_lshl_add_u64 v[0:1], s[8:9], 2, v[0:1]
	v_lshl_add_u64 v[0:1], v[0:1], 0, v[170:171]
	s_add_i32 m0, s3, 0x22000
	v_readlane_b32 s8, v252, 31
	global_load_lds_dwordx4 v[0:1], off
	v_mov_b32_e32 v123, 0
	v_readlane_b32 s9, v252, 32
	s_andn2_b64 vcc, exec, s[8:9]
	s_waitcnt vmcnt(0)
	s_cbranch_vccnz .LBB0_3996
	s_add_u32 s4, s4, 0x20080
	s_addc_u32 s5, s5, 0
	s_add_u32 s25, s6, 0x100
	v_mov_b32_e32 v0, 0
	s_addc_u32 s27, s7, 0
	s_mov_b32 s6, 0
	.p2align 6
.Lpeel_5:
	s_add_i32 s34, s6, 2
	s_add_u32 s8, s4, 0xfffe0080
	s_addc_u32 s7, s5, -1
	s_add_i32 s30, 0, 0x10000
	v_add_u32_e32 v140, s30, v200
	ds_read_b128 v[128:131], v140
	ds_read_b128 v[132:135], v140 offset:1024
	ds_read_b128 v[136:139], v140 offset:2048
	ds_read_b128 v[140:143], v140 offset:3072
	s_cmp_eq_u32 s12, s6
	s_cselect_b32 s6, s52, s8
	s_cselect_b32 s7, s53, s7
	s_cselect_b32 s9, s55, s27
	s_cselect_b32 s8, s54, s25
	v_mov_b32_e32 v168, v169
	ds_read_b128 v[144:147], v182
	ds_read_b128 v[148:151], v182 offset:1024
	ds_read_b128 v[152:155], v182 offset:2048
	ds_read_b128 v[156:159], v182 offset:3072
	ds_read_b128 v[160:163], v182 offset:4096
	ds_read_b128 v[164:167], v182 offset:5120
	ds_read_b128 v[184:187], v182 offset:6144
	ds_read_b128 v[188:191], v182 offset:7168
	s_nop 0
	v_mov_b32_e32 v168, v181
	s_nop 0
	s_waitcnt lgkmcnt(8)
	s_barrier
	s_waitcnt lgkmcnt(0)
	s_setprio 1
	s_waitcnt lgkmcnt(0)
	v_mfma_scale_f32_16x16x128_f8f6f4 v[120:123], v[128:135], v[144:151], 0, v183, v183 op_sel_hi:[0,0,0]
	v_mov_b32_e32 v170, v200
	v_mfma_scale_f32_16x16x128_f8f6f4 v[124:127], v[136:143], v[144:151], 0, v183, v183 op_sel_hi:[0,0,0]
	s_add_i32 m0, s3, 0xc000
	v_mfma_scale_f32_16x16x128_f8f6f4 v[200:203], v[136:143], v[160:167], 0, v183, v183 op_sel_hi:[0,0,0]
	global_load_lds_dwordx4 v169, s[4:5]
	v_mfma_scale_f32_16x16x128_f8f6f4 v[176:179], v[128:135], v[152:159], 0, v183, v183 op_sel_hi:[0,0,0]
	v_mfma_scale_f32_16x16x128_f8f6f4 v[192:195], v[136:143], v[152:159], 0, v183, v183 op_sel_hi:[0,0,0]
	s_add_i32 m0, s3, 0xe000
	v_mfma_scale_f32_16x16x128_f8f6f4 v[196:199], v[128:135], v[160:167], 0, v183, v183 op_sel_hi:[0,0,0]
	global_load_lds_dwordx4 v181, s[4:5]
	v_mfma_scale_f32_16x16x128_f8f6f4 v[204:207], v[128:135], v[184:191], 0, v183, v183 op_sel_hi:[0,0,0]
	v_mfma_scale_f32_16x16x128_f8f6f4 v[208:211], v[136:143], v[184:191], 0, v183, v183 op_sel_hi:[0,0,0]
	s_setprio 0
	s_barrier
	s_add_i32 s35, 0, 0x14000
	s_nop 1
	v_add_u32_e32 v92, s35, v170
	v_mov_b32_e32 v104, v180
	s_add_i32 s30, s30, s33
	ds_read_b128 v[72:75], v92
	ds_read_b128 v[76:79], v92 offset:1024
	ds_read_b128 v[88:91], v92 offset:2048
	ds_read_b128 v[92:95], v92 offset:3072
	s_mov_b32 m0, s30
	s_nop 0
	global_load_lds_dwordx4 v104, s[8:9]
	v_mov_b32_e32 v104, v212
	s_add_i32 m0, s30, 0x2000
	s_nop 0
	global_load_lds_dwordx4 v104, s[8:9]
	s_barrier
	s_waitcnt lgkmcnt(0)
	s_setprio 1
	s_waitcnt lgkmcnt(0)
	v_mfma_scale_f32_16x16x128_f8f6f4 v[116:119], v[144:151], v[72:79], 0, v183, v183 op_sel_hi:[0,0,0]
	v_mov_b32_e32 v168, v212
	v_mfma_scale_f32_16x16x128_f8f6f4 v[112:115], v[144:151], v[88:95], 0, v183, v183 op_sel_hi:[0,0,0]
	v_mfma_scale_f32_16x16x128_f8f6f4 v[212:215], v[152:159], v[72:79], 0, v183, v183 op_sel_hi:[0,0,0]
	v_mfma_scale_f32_16x16x128_f8f6f4 v[216:219], v[152:159], v[88:95], 0, v183, v183 op_sel_hi:[0,0,0]
	v_mfma_scale_f32_16x16x128_f8f6f4 v[220:223], v[160:167], v[72:79], 0, v183, v183 op_sel_hi:[0,0,0]
	v_mfma_scale_f32_16x16x128_f8f6f4 v[160:163], v[160:167], v[88:95], 0, v183, v183 op_sel_hi:[0,0,0]
	v_mfma_scale_f32_16x16x128_f8f6f4 v[164:167], v[184:191], v[72:79], 0, v183, v183 op_sel_hi:[0,0,0]
	v_mfma_scale_f32_16x16x128_f8f6f4 v[184:187], v[184:191], v[88:95], 0, v183, v183 op_sel_hi:[0,0,0]
	s_setprio 0
	v_mov_b32_e32 v144, v169
	s_barrier
	s_nop 2
	ds_read_b128 v[64:67], v182 offset:16384
	ds_read_b128 v[68:71], v182 offset:17408
	ds_read_b128 v[80:83], v182 offset:18432
	ds_read_b128 v[84:87], v182 offset:19456
	ds_read_b128 v[96:99], v182 offset:20480
	ds_read_b128 v[100:103], v182 offset:21504
	ds_read_b128 v[104:107], v182 offset:22528
	ds_read_b128 v[108:111], v182 offset:23552
	s_nop 0
	v_mov_b32_e32 v144, v181
	s_nop 0
	s_barrier
	s_waitcnt lgkmcnt(0)
	s_setprio 1
	s_waitcnt lgkmcnt(0)
	v_mfma_scale_f32_16x16x128_f8f6f4 v[224:227], v[128:135], v[64:71], 0, v183, v183 op_sel_hi:[0,0,0]
	v_mfma_scale_f32_16x16x128_f8f6f4 v[228:231], v[136:143], v[64:71], 0, v183, v183 op_sel_hi:[0,0,0]
	s_mov_b32 m0, s3
	v_mfma_scale_f32_16x16x128_f8f6f4 v[232:235], v[128:135], v[80:87], 0, v183, v183 op_sel_hi:[0,0,0]
	global_load_lds_dwordx4 v169, s[6:7]
	v_mfma_scale_f32_16x16x128_f8f6f4 v[236:239], v[136:143], v[80:87], 0, v183, v183 op_sel_hi:[0,0,0]
	v_mfma_scale_f32_16x16x128_f8f6f4 v[240:243], v[128:135], v[96:103], 0, v183, v183 op_sel_hi:[0,0,0]
	s_mov_b32 m0, s11
	v_mfma_scale_f32_16x16x128_f8f6f4 v[244:247], v[136:143], v[96:103], 0, v183, v183 op_sel_hi:[0,0,0]
	global_load_lds_dwordx4 v181, s[6:7]
	v_mfma_scale_f32_16x16x128_f8f6f4 v[248:251], v[128:135], v[104:111], 0, v183, v183 op_sel_hi:[0,0,0]
	v_mfma_scale_f32_16x16x128_f8f6f4 v[172:175], v[136:143], v[104:111], 0, v183, v183 op_sel_hi:[0,0,0]
	s_setprio 0
	s_barrier
	s_add_u32 s30, s8, s20
	s_addc_u32 s31, s9, s21
	s_nop 2
	v_mov_b32_e32 v8, v180
	s_add_i32 s35, s35, s33
	s_mov_b32 s100, s35
	s_nop 0
	v_mov_b32_e32 v8, v168
	s_add_i32 s101, s35, 0x2000
	s_nop 0
	s_waitcnt vmcnt(4)
	s_barrier
	s_setprio 1
	v_mfma_scale_f32_16x16x128_f8f6f4 v[52:55], v[64:71], v[72:79], 0, v183, v183 op_sel_hi:[0,0,0]
	v_mfma_scale_f32_16x16x128_f8f6f4 v[48:51], v[64:71], v[88:95], 0, v183, v183 op_sel_hi:[0,0,0]
	s_mov_b32 m0, s100
	v_mfma_scale_f32_16x16x128_f8f6f4 v[36:39], v[80:87], v[72:79], 0, v183, v183 op_sel_hi:[0,0,0]
	global_load_lds_dwordx4 v180, s[30:31]
	v_mfma_scale_f32_16x16x128_f8f6f4 v[32:35], v[80:87], v[88:95], 0, v183, v183 op_sel_hi:[0,0,0]
	v_mfma_scale_f32_16x16x128_f8f6f4 v[20:23], v[96:103], v[72:79], 0, v183, v183 op_sel_hi:[0,0,0]
	s_mov_b32 m0, s101
	v_mfma_scale_f32_16x16x128_f8f6f4 v[16:19], v[96:103], v[88:95], 0, v183, v183 op_sel_hi:[0,0,0]
	global_load_lds_dwordx4 v168, s[30:31]
	v_mfma_scale_f32_16x16x128_f8f6f4 v[4:7], v[104:111], v[72:79], 0, v183, v183 op_sel_hi:[0,0,0]
	v_mfma_scale_f32_16x16x128_f8f6f4 v[0:3], v[104:111], v[88:95], 0, v183, v183 op_sel_hi:[0,0,0]
	s_setprio 0
	s_add_i32 s35, 0, 0x18000
	v_add_u32_e32 v24, s35, v170
	s_barrier
	ds_read_b128 v[8:11], v24
	ds_read_b128 v[12:15], v24 offset:1024
	ds_read_b128 v[128:131], v24 offset:2048
	ds_read_b128 v[132:135], v24 offset:3072
	s_add_u32 s36, s6, 0x20000
	v_mov_b32_e32 v64, v169
	ds_read_b128 v[24:27], v182 offset:32768
	ds_read_b128 v[28:31], v182 offset:33792
	ds_read_b128 v[40:43], v182 offset:34816
	ds_read_b128 v[44:47], v182 offset:35840
	ds_read_b128 v[56:59], v182 offset:36864
	ds_read_b128 v[60:63], v182 offset:37888
	ds_read_b128 v[136:139], v182 offset:38912
	ds_read_b128 v[140:143], v182 offset:39936
	s_addc_u32 s37, s7, 0
	s_nop 0
	v_mov_b32_e32 v64, v181
	s_nop 0
	s_waitcnt lgkmcnt(8)
	s_barrier
	s_waitcnt lgkmcnt(0)
	s_setprio 1
	s_waitcnt lgkmcnt(0)
	v_mfma_scale_f32_16x16x128_f8f6f4 v[120:123], v[8:15], v[24:31], v[120:123], v183, v183 op_sel_hi:[0,0,0]
	v_mfma_scale_f32_16x16x128_f8f6f4 v[124:127], v[128:135], v[24:31], v[124:127], v183, v183 op_sel_hi:[0,0,0]
	s_mov_b32 m0, s14
	v_mfma_scale_f32_16x16x128_f8f6f4 v[108:111], v[8:15], v[40:47], v[176:179], v183, v183 op_sel_hi:[0,0,0]
	global_load_lds_dwordx4 v169, s[36:37]
	v_mfma_scale_f32_16x16x128_f8f6f4 v[104:107], v[128:135], v[40:47], v[192:195], v183, v183 op_sel_hi:[0,0,0]
	v_mfma_scale_f32_16x16x128_f8f6f4 v[92:95], v[8:15], v[56:63], v[196:199], v183, v183 op_sel_hi:[0,0,0]
	s_mov_b32 m0, s15
	v_mfma_scale_f32_16x16x128_f8f6f4 v[88:91], v[128:135], v[56:63], v[200:203], v183, v183 op_sel_hi:[0,0,0]
	global_load_lds_dwordx4 v181, s[36:37]
	v_mfma_scale_f32_16x16x128_f8f6f4 v[76:79], v[8:15], v[136:143], v[204:207], v183, v183 op_sel_hi:[0,0,0]
	s_nop 5
	v_mov_b32_e32 v200, v170
	v_mfma_scale_f32_16x16x128_f8f6f4 v[72:75], v[128:135], v[136:143], v[208:211], v183, v183 op_sel_hi:[0,0,0]
	s_setprio 0
	s_barrier
	s_add_i32 s36, 0, 0x1c000
	v_add_u32_e32 v64, s36, v200
	v_mov_b32_e32 v170, v180
	ds_read_b128 v[144:147], v64
	ds_read_b128 v[148:151], v64 offset:1024
	ds_read_b128 v[152:155], v64 offset:2048
	ds_read_b128 v[156:159], v64 offset:3072
	s_add_i32 s35, s35, s33
	v_lshl_add_u64 v[64:65], s[8:9], 0, v[170:171]
	v_lshl_add_u64 v[64:65], v[64:65], 0, s[62:63]
	v_mov_b32_e32 v170, v168
	v_lshl_add_u64 v[64:65], s[8:9], 0, v[170:171]
	v_lshl_add_u64 v[64:65], v[64:65], 0, s[62:63]
	s_barrier
	s_waitcnt lgkmcnt(0)
	s_setprio 1
	s_waitcnt lgkmcnt(0)
	v_mfma_scale_f32_16x16x128_f8f6f4 v[116:119], v[24:31], v[144:151], v[116:119], v183, v183 op_sel_hi:[0,0,0]
	v_mfma_scale_f32_16x16x128_f8f6f4 v[112:115], v[24:31], v[152:159], v[112:115], v183, v183 op_sel_hi:[0,0,0]
	s_add_u32 s98, s8, s62
	s_addc_u32 s99, s9, s63
	s_mov_b32 m0, s35
	v_mfma_scale_f32_16x16x128_f8f6f4 v[100:103], v[40:47], v[144:151], v[212:215], v183, v183 op_sel_hi:[0,0,0]
	global_load_lds_dwordx4 v180, s[98:99]
	v_mfma_scale_f32_16x16x128_f8f6f4 v[96:99], v[40:47], v[152:159], v[216:219], v183, v183 op_sel_hi:[0,0,0]
	s_nop 5
	v_mov_b32_e32 v212, v168
	v_mfma_scale_f32_16x16x128_f8f6f4 v[84:87], v[56:63], v[144:151], v[220:223], v183, v183 op_sel_hi:[0,0,0]
	s_add_i32 m0, s35, 0x2000
	v_mfma_scale_f32_16x16x128_f8f6f4 v[80:83], v[56:63], v[152:159], v[160:163], v183, v183 op_sel_hi:[0,0,0]
	global_load_lds_dwordx4 v168, s[98:99]
	v_mfma_scale_f32_16x16x128_f8f6f4 v[68:71], v[136:143], v[144:151], v[164:167], v183, v183 op_sel_hi:[0,0,0]
	v_mfma_scale_f32_16x16x128_f8f6f4 v[64:67], v[136:143], v[152:159], v[184:187], v183, v183 op_sel_hi:[0,0,0]
	s_setprio 0
	v_mov_b32_e32 v170, v169
	s_barrier
	ds_read_b128 v[136:139], v182 offset:49152
	ds_read_b128 v[140:143], v182 offset:50176
	ds_read_b128 v[160:163], v182 offset:51200
	ds_read_b128 v[164:167], v182 offset:52224
	ds_read_b128 v[184:187], v182 offset:53248
	ds_read_b128 v[188:191], v182 offset:54272
	ds_read_b128 v[192:195], v182 offset:55296
	ds_read_b128 v[196:199], v182 offset:56320
	v_lshl_add_u64 v[24:25], s[6:7], 0, v[170:171]
	v_lshl_add_u64 v[24:25], v[24:25], 0, s[62:63]
	v_mov_b32_e32 v170, v181
	v_lshl_add_u64 v[24:25], s[6:7], 0, v[170:171]
	v_lshl_add_u64 v[24:25], v[24:25], 0, s[62:63]
	s_barrier
	s_waitcnt lgkmcnt(0)
	s_setprio 1
	s_waitcnt lgkmcnt(0)
	v_mfma_scale_f32_16x16x128_f8f6f4 v[60:63], v[8:15], v[136:143], v[224:227], v183, v183 op_sel_hi:[0,0,0]
	v_mfma_scale_f32_16x16x128_f8f6f4 v[56:59], v[128:135], v[136:143], v[228:231], v183, v183 op_sel_hi:[0,0,0]
	s_add_u32 s98, s6, s62
	s_addc_u32 s99, s7, s63
	s_mov_b32 m0, s16
	v_mfma_scale_f32_16x16x128_f8f6f4 v[44:47], v[8:15], v[160:167], v[232:235], v183, v183 op_sel_hi:[0,0,0]
	global_load_lds_dwordx4 v169, s[98:99]
	v_mfma_scale_f32_16x16x128_f8f6f4 v[40:43], v[128:135], v[160:167], v[236:239], v183, v183 op_sel_hi:[0,0,0]
	v_mfma_scale_f32_16x16x128_f8f6f4 v[28:31], v[8:15], v[184:191], v[240:243], v183, v183 op_sel_hi:[0,0,0]
	s_mov_b32 m0, s17
	v_mfma_scale_f32_16x16x128_f8f6f4 v[24:27], v[128:135], v[184:191], v[244:247], v183, v183 op_sel_hi:[0,0,0]
	global_load_lds_dwordx4 v181, s[98:99]
	v_mfma_scale_f32_16x16x128_f8f6f4 v[12:15], v[8:15], v[192:199], v[248:251], v183, v183 op_sel_hi:[0,0,0]
	v_mfma_scale_f32_16x16x128_f8f6f4 v[8:11], v[128:135], v[192:199], v[172:175], v183, v183 op_sel_hi:[0,0,0]
	s_setprio 0
	s_barrier
	v_mov_b32_e32 v170, v180
	s_add_i32 s6, s36, s33
	v_lshl_add_u64 v[128:129], s[30:31], 0, v[170:171]
	v_lshl_add_u64 v[128:129], v[128:129], 0, s[62:63]
	s_mov_b32 s100, s6
	v_mov_b32_e32 v170, v168
	s_add_i32 s101, s6, 0x2000
	v_lshl_add_u64 v[128:129], s[30:31], 0, v[170:171]
	v_lshl_add_u64 v[128:129], v[128:129], 0, s[62:63]
	s_waitcnt vmcnt(4)
	s_barrier
	s_setprio 1
	v_mfma_scale_f32_16x16x128_f8f6f4 v[52:55], v[136:143], v[144:151], v[52:55], v183, v183 op_sel_hi:[0,0,0]
	v_mfma_scale_f32_16x16x128_f8f6f4 v[48:51], v[136:143], v[152:159], v[48:51], v183, v183 op_sel_hi:[0,0,0]
	s_add_u32 s98, s30, s62
	s_addc_u32 s99, s31, s63
	s_mov_b32 m0, s100
	v_mfma_scale_f32_16x16x128_f8f6f4 v[36:39], v[160:167], v[144:151], v[36:39], v183, v183 op_sel_hi:[0,0,0]
	global_load_lds_dwordx4 v180, s[98:99]
	v_mfma_scale_f32_16x16x128_f8f6f4 v[32:35], v[160:167], v[152:159], v[32:35], v183, v183 op_sel_hi:[0,0,0]
	v_mfma_scale_f32_16x16x128_f8f6f4 v[20:23], v[184:191], v[144:151], v[20:23], v183, v183 op_sel_hi:[0,0,0]
	s_mov_b32 m0, s101
	v_mfma_scale_f32_16x16x128_f8f6f4 v[16:19], v[184:191], v[152:159], v[16:19], v183, v183 op_sel_hi:[0,0,0]
	global_load_lds_dwordx4 v168, s[98:99]
	v_mfma_scale_f32_16x16x128_f8f6f4 v[4:7], v[192:199], v[144:151], v[4:7], v183, v183 op_sel_hi:[0,0,0]
	v_mfma_scale_f32_16x16x128_f8f6f4 v[0:3], v[192:199], v[152:159], v[0:3], v183, v183 op_sel_hi:[0,0,0]
	s_setprio 0
	s_add_u32 s4, s4, 0x100
	s_addc_u32 s5, s5, 0
	s_add_u32 s25, s25, 0x100
	s_addc_u32 s27, s27, 0
	s_cmp_ge_i32 s34, s13
	s_mov_b32 s6, s34
	s_barrier
	s_cbranch_scc0 .LBB0_3995
	s_branch .Lpeel_exit_5
	.p2align 6

.LBB0_4064:
	v_mbcnt_lo_u32_b32 v2, -1, 0
	v_mbcnt_hi_u32_b32 v2, -1, v2
	s_lshl_b32 s22, s10, 8
	v_add_u32_e32 v0, s58, v2
	v_ashrrev_i32_e32 v0, 1, v0
	v_add_u32_e32 v0, s22, v0
	v_ashrrev_i32_e32 v1, 31, v0
	v_readlane_b32 s8, v253, 54
	v_lshlrev_b64 v[0:1], 6, v[0:1]
	v_readlane_b32 s9, v253, 55
	v_lshlrev_b32_e32 v2, 4, v2
	v_and_b32_e32 v170, 16, v2
	v_lshl_add_u64 v[0:1], s[8:9], 0, v[0:1]
	s_lshl_b32 s8, s23, 3
	s_ashr_i32 s9, s8, 31
	v_lshl_add_u64 v[0:1], s[8:9], 2, v[0:1]
	v_lshl_add_u64 v[0:1], v[0:1], 0, v[170:171]
	s_add_i32 m0, s3, 0x22000
	v_readlane_b32 s8, v252, 31
	global_load_lds_dwordx4 v[0:1], off
	v_mov_b32_e32 v123, 0
	v_readlane_b32 s9, v252, 32
	s_andn2_b64 vcc, exec, s[8:9]
	s_waitcnt vmcnt(0)
	s_waitcnt vmcnt(0)
	s_cbranch_vccnz .LBB0_4067
	s_add_u32 s4, s4, 0x20080
	s_addc_u32 s5, s5, 0
	s_add_u32 s25, s6, 0x100
	v_mov_b32_e32 v0, 0
	s_addc_u32 s27, s7, 0
	s_mov_b32 s6, 0
	.p2align 6
.Lpeel_6:
	s_add_i32 s34, s6, 2
	s_add_u32 s8, s4, 0xfffe0080
	s_addc_u32 s7, s5, -1
	s_add_i32 s30, 0, 0x10000
	v_add_u32_e32 v140, s30, v181
	ds_read_b128 v[128:131], v140
	ds_read_b128 v[132:135], v140 offset:1024
	ds_read_b128 v[136:139], v140 offset:2048
	ds_read_b128 v[140:143], v140 offset:3072
	s_cmp_eq_u32 s12, s6
	s_cselect_b32 s6, s52, s8
	s_cselect_b32 s7, s53, s7
	s_cselect_b32 s9, s55, s27
	s_cselect_b32 s8, s54, s25
	v_mov_b32_e32 v168, v169
	ds_read_b128 v[144:147], v182
	ds_read_b128 v[148:151], v182 offset:1024
	ds_read_b128 v[152:155], v182 offset:2048
	ds_read_b128 v[156:159], v182 offset:3072
	ds_read_b128 v[160:163], v182 offset:4096
	ds_read_b128 v[164:167], v182 offset:5120
	ds_read_b128 v[184:187], v182 offset:6144
	ds_read_b128 v[188:191], v182 offset:7168
	s_add_i32 m0, s3, 0xc000
	s_nop 0
	global_load_lds_dwordx4 v168, s[4:5]
	v_mov_b32_e32 v168, v200
	s_add_i32 m0, s3, 0xe000
	s_nop 0
	global_load_lds_dwordx4 v168, s[4:5]
	s_waitcnt lgkmcnt(8)
	s_barrier
	s_waitcnt lgkmcnt(0)
	s_setprio 1
	s_waitcnt lgkmcnt(0)
	v_mfma_scale_f32_16x16x128_f8f6f4 v[120:123], v[128:135], v[144:151], 0, v183, v183 op_sel_hi:[0,0,0]
	v_mov_b32_e32 v170, v200
	v_mfma_scale_f32_16x16x128_f8f6f4 v[124:127], v[136:143], v[144:151], 0, v183, v183 op_sel_hi:[0,0,0]
	v_mfma_scale_f32_16x16x128_f8f6f4 v[200:203], v[128:135], v[160:167], 0, v183, v183 op_sel_hi:[0,0,0]
	v_mfma_scale_f32_16x16x128_f8f6f4 v[192:195], v[128:135], v[152:159], 0, v183, v183 op_sel_hi:[0,0,0]
	v_mfma_scale_f32_16x16x128_f8f6f4 v[196:199], v[136:143], v[152:159], 0, v183, v183 op_sel_hi:[0,0,0]
	v_mfma_scale_f32_16x16x128_f8f6f4 v[204:207], v[136:143], v[160:167], 0, v183, v183 op_sel_hi:[0,0,0]
	v_mfma_scale_f32_16x16x128_f8f6f4 v[208:211], v[128:135], v[184:191], 0, v183, v183 op_sel_hi:[0,0,0]
	v_mfma_scale_f32_16x16x128_f8f6f4 v[212:215], v[136:143], v[184:191], 0, v183, v183 op_sel_hi:[0,0,0]
	s_setprio 0
	s_barrier
	s_add_i32 s35, 0, 0x14000
	v_add_u32_e32 v92, s35, v181
	v_mov_b32_e32 v104, v216
	s_add_i32 s30, s30, s33
	s_nop 0
	ds_read_b128 v[72:75], v92
	ds_read_b128 v[76:79], v92 offset:1024
	ds_read_b128 v[88:91], v92 offset:2048
	ds_read_b128 v[92:95], v92 offset:3072
	s_mov_b32 m0, s30
	s_nop 0
	global_load_lds_dwordx4 v104, s[8:9]
	v_mov_b32_e32 v104, v180
	s_add_i32 m0, s30, 0x2000
	s_nop 0
	global_load_lds_dwordx4 v104, s[8:9]
	s_barrier
	s_waitcnt lgkmcnt(0)
	s_setprio 1
	s_waitcnt lgkmcnt(0)
	v_mfma_scale_f32_16x16x128_f8f6f4 v[116:119], v[72:79], v[144:151], 0, v183, v183 op_sel_hi:[0,0,0]
	v_mov_b32_e32 v168, v216
	v_mfma_scale_f32_16x16x128_f8f6f4 v[112:115], v[88:95], v[144:151], 0, v183, v183 op_sel_hi:[0,0,0]
	v_mfma_scale_f32_16x16x128_f8f6f4 v[216:219], v[72:79], v[152:159], 0, v183, v183 op_sel_hi:[0,0,0]
	v_mfma_scale_f32_16x16x128_f8f6f4 v[220:223], v[88:95], v[152:159], 0, v183, v183 op_sel_hi:[0,0,0]
	v_mfma_scale_f32_16x16x128_f8f6f4 v[224:227], v[72:79], v[160:167], 0, v183, v183 op_sel_hi:[0,0,0]
	v_mfma_scale_f32_16x16x128_f8f6f4 v[160:163], v[88:95], v[160:167], 0, v183, v183 op_sel_hi:[0,0,0]
	v_mfma_scale_f32_16x16x128_f8f6f4 v[164:167], v[72:79], v[184:191], 0, v183, v183 op_sel_hi:[0,0,0]
	v_mfma_scale_f32_16x16x128_f8f6f4 v[184:187], v[88:95], v[184:191], 0, v183, v183 op_sel_hi:[0,0,0]
	s_setprio 0
	v_mov_b32_e32 v144, v169
	s_barrier
	s_nop 2
	ds_read_b128 v[64:67], v182 offset:16384
	ds_read_b128 v[68:71], v182 offset:17408
	ds_read_b128 v[80:83], v182 offset:18432
	ds_read_b128 v[84:87], v182 offset:19456
	ds_read_b128 v[96:99], v182 offset:20480
	ds_read_b128 v[100:103], v182 offset:21504
	ds_read_b128 v[104:107], v182 offset:22528
	ds_read_b128 v[108:111], v182 offset:23552
	s_nop 0
	v_mov_b32_e32 v144, v170
	s_nop 0
	s_barrier
	s_waitcnt lgkmcnt(0)
	s_setprio 1
	s_waitcnt lgkmcnt(0)
	v_mfma_scale_f32_16x16x128_f8f6f4 v[228:231], v[128:135], v[64:71], 0, v183, v183 op_sel_hi:[0,0,0]
	v_mfma_scale_f32_16x16x128_f8f6f4 v[232:235], v[136:143], v[64:71], 0, v183, v183 op_sel_hi:[0,0,0]
	s_mov_b32 m0, s3
	v_mfma_scale_f32_16x16x128_f8f6f4 v[236:239], v[128:135], v[80:87], 0, v183, v183 op_sel_hi:[0,0,0]
	global_load_lds_dwordx4 v169, s[6:7]
	v_mfma_scale_f32_16x16x128_f8f6f4 v[240:243], v[136:143], v[80:87], 0, v183, v183 op_sel_hi:[0,0,0]
	v_mfma_scale_f32_16x16x128_f8f6f4 v[244:247], v[128:135], v[96:103], 0, v183, v183 op_sel_hi:[0,0,0]
	s_mov_b32 m0, s11
	v_mfma_scale_f32_16x16x128_f8f6f4 v[248:251], v[136:143], v[96:103], 0, v183, v183 op_sel_hi:[0,0,0]
	global_load_lds_dwordx4 v170, s[6:7]
	v_mfma_scale_f32_16x16x128_f8f6f4 v[172:175], v[128:135], v[104:111], 0, v183, v183 op_sel_hi:[0,0,0]
	v_mfma_scale_f32_16x16x128_f8f6f4 v[176:179], v[136:143], v[104:111], 0, v183, v183 op_sel_hi:[0,0,0]
	s_setprio 0
	s_barrier
	s_add_u32 s30, s8, s20
	s_addc_u32 s31, s9, s21
	s_nop 2
	v_mov_b32_e32 v8, v168
	s_add_i32 s35, s35, s33
	s_mov_b32 s100, s35
	s_nop 0
	v_mov_b32_e32 v8, v180
	s_add_i32 s101, s35, 0x2000
	s_nop 0
	s_waitcnt vmcnt(4)
	s_barrier
	s_setprio 1
	v_mfma_scale_f32_16x16x128_f8f6f4 v[52:55], v[72:79], v[64:71], 0, v183, v183 op_sel_hi:[0,0,0]
	v_mfma_scale_f32_16x16x128_f8f6f4 v[48:51], v[88:95], v[64:71], 0, v183, v183 op_sel_hi:[0,0,0]
	s_mov_b32 m0, s100
	v_mfma_scale_f32_16x16x128_f8f6f4 v[36:39], v[72:79], v[80:87], 0, v183, v183 op_sel_hi:[0,0,0]
	global_load_lds_dwordx4 v168, s[30:31]
	v_mfma_scale_f32_16x16x128_f8f6f4 v[32:35], v[88:95], v[80:87], 0, v183, v183 op_sel_hi:[0,0,0]
	v_mfma_scale_f32_16x16x128_f8f6f4 v[20:23], v[72:79], v[96:103], 0, v183, v183 op_sel_hi:[0,0,0]
	s_mov_b32 m0, s101
	v_mfma_scale_f32_16x16x128_f8f6f4 v[16:19], v[88:95], v[96:103], 0, v183, v183 op_sel_hi:[0,0,0]
	global_load_lds_dwordx4 v180, s[30:31]
	v_mfma_scale_f32_16x16x128_f8f6f4 v[4:7], v[72:79], v[104:111], 0, v183, v183 op_sel_hi:[0,0,0]
	v_mfma_scale_f32_16x16x128_f8f6f4 v[0:3], v[88:95], v[104:111], 0, v183, v183 op_sel_hi:[0,0,0]
	s_setprio 0
	s_add_i32 s35, 0, 0x18000
	v_add_u32_e32 v24, s35, v181
	s_barrier
	ds_read_b128 v[8:11], v24
	ds_read_b128 v[12:15], v24 offset:1024
	ds_read_b128 v[128:131], v24 offset:2048
	ds_read_b128 v[132:135], v24 offset:3072
	s_add_u32 s36, s6, 0x20000
	v_mov_b32_e32 v64, v169
	ds_read_b128 v[24:27], v182 offset:32768
	ds_read_b128 v[28:31], v182 offset:33792
	ds_read_b128 v[40:43], v182 offset:34816
	ds_read_b128 v[44:47], v182 offset:35840
	ds_read_b128 v[56:59], v182 offset:36864
	ds_read_b128 v[60:63], v182 offset:37888
	ds_read_b128 v[136:139], v182 offset:38912
	ds_read_b128 v[140:143], v182 offset:39936
	s_addc_u32 s37, s7, 0
	s_nop 0
	v_mov_b32_e32 v64, v170
	s_nop 0
	s_waitcnt lgkmcnt(8)
	s_barrier
	s_waitcnt lgkmcnt(0)
	s_setprio 1
	s_waitcnt lgkmcnt(0)
	v_mfma_scale_f32_16x16x128_f8f6f4 v[120:123], v[8:15], v[24:31], v[120:123], v183, v183 op_sel_hi:[0,0,0]
	v_mfma_scale_f32_16x16x128_f8f6f4 v[124:127], v[128:135], v[24:31], v[124:127], v183, v183 op_sel_hi:[0,0,0]
	s_mov_b32 m0, s14
	v_mfma_scale_f32_16x16x128_f8f6f4 v[108:111], v[8:15], v[40:47], v[192:195], v183, v183 op_sel_hi:[0,0,0]
	global_load_lds_dwordx4 v169, s[36:37]
	v_mfma_scale_f32_16x16x128_f8f6f4 v[104:107], v[128:135], v[40:47], v[196:199], v183, v183 op_sel_hi:[0,0,0]
	v_mfma_scale_f32_16x16x128_f8f6f4 v[92:95], v[8:15], v[56:63], v[200:203], v183, v183 op_sel_hi:[0,0,0]
	s_mov_b32 m0, s15
	v_mfma_scale_f32_16x16x128_f8f6f4 v[88:91], v[128:135], v[56:63], v[204:207], v183, v183 op_sel_hi:[0,0,0]
	global_load_lds_dwordx4 v170, s[36:37]
	s_nop 5
	v_mov_b32_e32 v200, v170
	v_mfma_scale_f32_16x16x128_f8f6f4 v[76:79], v[8:15], v[136:143], v[208:211], v183, v183 op_sel_hi:[0,0,0]
	v_mfma_scale_f32_16x16x128_f8f6f4 v[72:75], v[128:135], v[136:143], v[212:215], v183, v183 op_sel_hi:[0,0,0]
	s_setprio 0
	s_barrier
	s_add_i32 s36, 0, 0x1c000
	v_add_u32_e32 v64, s36, v181
	v_mov_b32_e32 v170, v168
	ds_read_b128 v[144:147], v64
	ds_read_b128 v[148:151], v64 offset:1024
	ds_read_b128 v[152:155], v64 offset:2048
	ds_read_b128 v[156:159], v64 offset:3072
	s_add_i32 s35, s35, s33
	v_lshl_add_u64 v[64:65], s[8:9], 0, v[170:171]
	v_lshl_add_u64 v[64:65], v[64:65], 0, s[62:63]
	v_mov_b32_e32 v170, v180
	v_lshl_add_u64 v[64:65], s[8:9], 0, v[170:171]
	v_lshl_add_u64 v[64:65], v[64:65], 0, s[62:63]
	s_barrier
	s_waitcnt lgkmcnt(0)
	s_setprio 1
	s_waitcnt lgkmcnt(0)
	v_mfma_scale_f32_16x16x128_f8f6f4 v[116:119], v[144:151], v[24:31], v[116:119], v183, v183 op_sel_hi:[0,0,0]
	v_mfma_scale_f32_16x16x128_f8f6f4 v[112:115], v[152:159], v[24:31], v[112:115], v183, v183 op_sel_hi:[0,0,0]
	s_add_u32 s98, s8, s62
	s_addc_u32 s99, s9, s63
	s_mov_b32 m0, s35
	v_mfma_scale_f32_16x16x128_f8f6f4 v[100:103], v[144:151], v[40:47], v[216:219], v183, v183 op_sel_hi:[0,0,0]
	global_load_lds_dwordx4 v168, s[98:99]
	v_mfma_scale_f32_16x16x128_f8f6f4 v[96:99], v[152:159], v[40:47], v[220:223], v183, v183 op_sel_hi:[0,0,0]
	s_nop 5
	v_mov_b32_e32 v216, v168
	v_mfma_scale_f32_16x16x128_f8f6f4 v[84:87], v[144:151], v[56:63], v[224:227], v183, v183 op_sel_hi:[0,0,0]
	s_add_i32 m0, s35, 0x2000
	v_mfma_scale_f32_16x16x128_f8f6f4 v[80:83], v[152:159], v[56:63], v[160:163], v183, v183 op_sel_hi:[0,0,0]
	global_load_lds_dwordx4 v180, s[98:99]
	v_mfma_scale_f32_16x16x128_f8f6f4 v[68:71], v[144:151], v[136:143], v[164:167], v183, v183 op_sel_hi:[0,0,0]
	v_mfma_scale_f32_16x16x128_f8f6f4 v[64:67], v[152:159], v[136:143], v[184:187], v183, v183 op_sel_hi:[0,0,0]
	s_setprio 0
	v_mov_b32_e32 v170, v169
	s_barrier
	ds_read_b128 v[136:139], v182 offset:49152
	ds_read_b128 v[140:143], v182 offset:50176
	ds_read_b128 v[160:163], v182 offset:51200
	ds_read_b128 v[164:167], v182 offset:52224
	ds_read_b128 v[184:187], v182 offset:53248
	ds_read_b128 v[188:191], v182 offset:54272
	ds_read_b128 v[192:195], v182 offset:55296
	ds_read_b128 v[196:199], v182 offset:56320
	v_lshl_add_u64 v[24:25], s[6:7], 0, v[170:171]
	v_lshl_add_u64 v[24:25], v[24:25], 0, s[62:63]
	v_mov_b32_e32 v170, v200
	v_lshl_add_u64 v[24:25], s[6:7], 0, v[170:171]
	v_lshl_add_u64 v[24:25], v[24:25], 0, s[62:63]
	s_barrier
	s_waitcnt lgkmcnt(0)
	s_setprio 1
	s_waitcnt lgkmcnt(0)
	v_mfma_scale_f32_16x16x128_f8f6f4 v[60:63], v[8:15], v[136:143], v[228:231], v183, v183 op_sel_hi:[0,0,0]
	v_mfma_scale_f32_16x16x128_f8f6f4 v[56:59], v[128:135], v[136:143], v[232:235], v183, v183 op_sel_hi:[0,0,0]
	s_add_u32 s98, s6, s62
	s_addc_u32 s99, s7, s63
	s_mov_b32 m0, s16
	v_mfma_scale_f32_16x16x128_f8f6f4 v[44:47], v[8:15], v[160:167], v[236:239], v183, v183 op_sel_hi:[0,0,0]
	global_load_lds_dwordx4 v169, s[98:99]
	v_mfma_scale_f32_16x16x128_f8f6f4 v[40:43], v[128:135], v[160:167], v[240:243], v183, v183 op_sel_hi:[0,0,0]
	v_mfma_scale_f32_16x16x128_f8f6f4 v[28:31], v[8:15], v[184:191], v[244:247], v183, v183 op_sel_hi:[0,0,0]
	s_mov_b32 m0, s17
	v_mfma_scale_f32_16x16x128_f8f6f4 v[24:27], v[128:135], v[184:191], v[248:251], v183, v183 op_sel_hi:[0,0,0]
	global_load_lds_dwordx4 v200, s[98:99]
	v_mfma_scale_f32_16x16x128_f8f6f4 v[12:15], v[8:15], v[192:199], v[172:175], v183, v183 op_sel_hi:[0,0,0]
	v_mfma_scale_f32_16x16x128_f8f6f4 v[8:11], v[128:135], v[192:199], v[176:179], v183, v183 op_sel_hi:[0,0,0]
	s_setprio 0
	s_barrier
	v_mov_b32_e32 v170, v168
	s_add_i32 s6, s36, s33
	v_lshl_add_u64 v[128:129], s[30:31], 0, v[170:171]
	v_lshl_add_u64 v[128:129], v[128:129], 0, s[62:63]
	s_mov_b32 s100, s6
	v_mov_b32_e32 v170, v180
	s_add_i32 s101, s6, 0x2000
	v_lshl_add_u64 v[128:129], s[30:31], 0, v[170:171]
	v_lshl_add_u64 v[128:129], v[128:129], 0, s[62:63]
	s_waitcnt vmcnt(4)
	s_barrier
	s_setprio 1
	v_mfma_scale_f32_16x16x128_f8f6f4 v[52:55], v[144:151], v[136:143], v[52:55], v183, v183 op_sel_hi:[0,0,0]
	v_mfma_scale_f32_16x16x128_f8f6f4 v[48:51], v[152:159], v[136:143], v[48:51], v183, v183 op_sel_hi:[0,0,0]
	s_add_u32 s98, s30, s62
	s_addc_u32 s99, s31, s63
	s_mov_b32 m0, s100
	v_mfma_scale_f32_16x16x128_f8f6f4 v[36:39], v[144:151], v[160:167], v[36:39], v183, v183 op_sel_hi:[0,0,0]
	global_load_lds_dwordx4 v168, s[98:99]
	v_mfma_scale_f32_16x16x128_f8f6f4 v[32:35], v[152:159], v[160:167], v[32:35], v183, v183 op_sel_hi:[0,0,0]
	v_mfma_scale_f32_16x16x128_f8f6f4 v[20:23], v[144:151], v[184:191], v[20:23], v183, v183 op_sel_hi:[0,0,0]
	s_mov_b32 m0, s101
	v_mfma_scale_f32_16x16x128_f8f6f4 v[16:19], v[152:159], v[184:191], v[16:19], v183, v183 op_sel_hi:[0,0,0]
	global_load_lds_dwordx4 v180, s[98:99]
	v_mfma_scale_f32_16x16x128_f8f6f4 v[4:7], v[144:151], v[192:199], v[4:7], v183, v183 op_sel_hi:[0,0,0]
	v_mfma_scale_f32_16x16x128_f8f6f4 v[0:3], v[152:159], v[192:199], v[0:3], v183, v183 op_sel_hi:[0,0,0]
	s_setprio 0
	s_add_u32 s4, s4, 0x100
	s_addc_u32 s5, s5, 0
	s_add_u32 s25, s25, 0x100
	s_addc_u32 s27, s27, 0
	s_cmp_ge_i32 s34, s13
	s_mov_b32 s6, s34
	s_barrier
	s_cbranch_scc0 .LBB0_4066
	s_branch .Lpeel_exit_6
	.p2align 6

.LBB0_4931:
	s_add_u32 s20, s20, 0x40080
	s_addc_u32 s21, s21, 0
	s_add_u32 s11, s22, 0x100
	v_mov_b32_e32 v0, 0
	s_addc_u32 s13, s23, 0
	s_mov_b32 s50, -2
	.p2align 6
.Lpeel_7:
	ds_read_b128 v[146:149], v141
	ds_read_b128 v[150:153], v141 offset:1024
	ds_read_b128 v[154:157], v141 offset:2048
	ds_read_b128 v[158:161], v141 offset:3072
	s_add_u32 s22, s20, 0xfffc0080
	s_addc_u32 s23, s21, -1
	s_cmp_eq_u32 s50, 12
	s_cselect_b32 s25, s15, s23
	s_cselect_b32 s24, s14, s22
	s_cselect_b32 s23, s17, s13
	s_cselect_b32 s22, s16, s11
	v_mov_b32_e32 v128, v138
	ds_read_b128 v[162:165], v142
	ds_read_b128 v[166:169], v142 offset:1024
	ds_read_b128 v[170:173], v142 offset:2048
	ds_read_b128 v[174:177], v142 offset:3072
	ds_read_b128 v[178:181], v142 offset:4096
	ds_read_b128 v[182:185], v142 offset:5120
	ds_read_b128 v[186:189], v142 offset:6144
	ds_read_b128 v[190:193], v142 offset:7168
	s_nop 0
	v_mov_b32_e32 v128, v139
	s_nop 0
	s_waitcnt lgkmcnt(8)
	s_barrier
	s_waitcnt lgkmcnt(0)
	s_setprio 1
	s_waitcnt lgkmcnt(0)
	v_mfma_scale_f32_16x16x128_f8f6f4 v[124:127], v[146:153], v[162:169], 0, v143, v143 op_sel_hi:[0,0,0]
	v_mfma_scale_f32_16x16x128_f8f6f4 v[120:123], v[154:161], v[162:169], 0, v143, v143 op_sel_hi:[0,0,0]
	s_add_i32 m0, s19, 0xc000
	v_mfma_scale_f32_16x16x128_f8f6f4 v[116:119], v[146:153], v[170:177], 0, v143, v143 op_sel_hi:[0,0,0]
	global_load_lds_dwordx4 v138, s[20:21]
	v_mfma_scale_f32_16x16x128_f8f6f4 v[112:115], v[154:161], v[170:177], 0, v143, v143 op_sel_hi:[0,0,0]
	v_mfma_scale_f32_16x16x128_f8f6f4 v[132:135], v[146:153], v[178:185], 0, v143, v143 op_sel_hi:[0,0,0]
	s_add_i32 m0, s19, 0xe000
	v_mfma_scale_f32_16x16x128_f8f6f4 v[194:197], v[154:161], v[178:185], 0, v143, v143 op_sel_hi:[0,0,0]
	global_load_lds_dwordx4 v139, s[20:21]
	v_mfma_scale_f32_16x16x128_f8f6f4 v[198:201], v[146:153], v[186:193], 0, v143, v143 op_sel_hi:[0,0,0]
	v_mfma_scale_f32_16x16x128_f8f6f4 v[202:205], v[154:161], v[186:193], 0, v143, v143 op_sel_hi:[0,0,0]
	s_setprio 0
	s_barrier
	v_mov_b32_e32 v128, v138
	s_add_i32 s51, s44, s28
	s_nop 2
	ds_read_b128 v[96:99], v144
	ds_read_b128 v[100:103], v144 offset:1024
	ds_read_b128 v[104:107], v144 offset:2048
	ds_read_b128 v[108:111], v144 offset:3072
	s_nop 0
	v_mov_b32_e32 v128, v139
	s_nop 0
	s_barrier
	s_waitcnt lgkmcnt(0)
	s_setprio 1
	s_waitcnt lgkmcnt(0)
	v_mfma_scale_f32_16x16x128_f8f6f4 v[206:209], v[96:103], v[162:169], 0, v143, v143 op_sel_hi:[0,0,0]
	v_mfma_scale_f32_16x16x128_f8f6f4 v[162:165], v[104:111], v[162:169], 0, v143, v143 op_sel_hi:[0,0,0]
	s_mov_b32 m0, s51
	v_mfma_scale_f32_16x16x128_f8f6f4 v[166:169], v[96:103], v[170:177], 0, v143, v143 op_sel_hi:[0,0,0]
	global_load_lds_dwordx4 v138, s[22:23]
	v_mfma_scale_f32_16x16x128_f8f6f4 v[170:173], v[104:111], v[170:177], 0, v143, v143 op_sel_hi:[0,0,0]
	v_mfma_scale_f32_16x16x128_f8f6f4 v[174:177], v[96:103], v[178:185], 0, v143, v143 op_sel_hi:[0,0,0]
	s_add_i32 m0, s51, 0x2000
	v_mfma_scale_f32_16x16x128_f8f6f4 v[178:181], v[104:111], v[178:185], 0, v143, v143 op_sel_hi:[0,0,0]
	global_load_lds_dwordx4 v139, s[22:23]
	v_mfma_scale_f32_16x16x128_f8f6f4 v[182:185], v[96:103], v[186:193], 0, v143, v143 op_sel_hi:[0,0,0]
	v_mfma_scale_f32_16x16x128_f8f6f4 v[186:189], v[104:111], v[186:193], 0, v143, v143 op_sel_hi:[0,0,0]
	s_setprio 0
	v_mov_b32_e32 v128, v138
	s_barrier
	s_nop 2
	ds_read_b128 v[32:35], v142 offset:16384
	ds_read_b128 v[36:39], v142 offset:17408
	ds_read_b128 v[40:43], v142 offset:18432
	ds_read_b128 v[44:47], v142 offset:19456
	ds_read_b128 v[48:51], v142 offset:20480
	ds_read_b128 v[52:55], v142 offset:21504
	ds_read_b128 v[56:59], v142 offset:22528
	ds_read_b128 v[60:63], v142 offset:23552
	s_nop 0
	v_mov_b32_e32 v128, v139
	s_nop 0
	s_barrier
	s_waitcnt lgkmcnt(0)
	s_setprio 1
	s_waitcnt lgkmcnt(0)
	v_mfma_scale_f32_16x16x128_f8f6f4 v[92:95], v[146:153], v[32:39], 0, v143, v143 op_sel_hi:[0,0,0]
	v_mfma_scale_f32_16x16x128_f8f6f4 v[88:91], v[154:161], v[32:39], 0, v143, v143 op_sel_hi:[0,0,0]
	s_mov_b32 m0, s19
	v_mfma_scale_f32_16x16x128_f8f6f4 v[84:87], v[146:153], v[40:47], 0, v143, v143 op_sel_hi:[0,0,0]
	global_load_lds_dwordx4 v138, s[24:25]
	v_mfma_scale_f32_16x16x128_f8f6f4 v[80:83], v[154:161], v[40:47], 0, v143, v143 op_sel_hi:[0,0,0]
	v_mfma_scale_f32_16x16x128_f8f6f4 v[76:79], v[146:153], v[48:55], 0, v143, v143 op_sel_hi:[0,0,0]
	s_mov_b32 m0, s29
	v_mfma_scale_f32_16x16x128_f8f6f4 v[72:75], v[154:161], v[48:55], 0, v143, v143 op_sel_hi:[0,0,0]
	global_load_lds_dwordx4 v139, s[24:25]
	v_mfma_scale_f32_16x16x128_f8f6f4 v[190:193], v[146:153], v[56:63], 0, v143, v143 op_sel_hi:[0,0,0]
	v_mfma_scale_f32_16x16x128_f8f6f4 v[210:213], v[154:161], v[56:63], 0, v143, v143 op_sel_hi:[0,0,0]
	s_setprio 0
	s_barrier
	s_add_u32 s52, s22, 0x40000
	s_addc_u32 s53, s23, 0
	s_nop 2
	v_mov_b32_e32 v64, v138
	s_add_i32 s51, s45, s28
	s_mov_b32 s100, s51
	s_nop 0
	v_mov_b32_e32 v64, v139
	s_add_i32 s101, s51, 0x2000
	s_nop 0
	s_waitcnt vmcnt(4)
	s_barrier
	s_setprio 1
	v_mfma_scale_f32_16x16x128_f8f6f4 v[214:217], v[96:103], v[32:39], 0, v143, v143 op_sel_hi:[0,0,0]
	v_mfma_scale_f32_16x16x128_f8f6f4 v[218:221], v[104:111], v[32:39], 0, v143, v143 op_sel_hi:[0,0,0]
	s_mov_b32 m0, s100
	v_mfma_scale_f32_16x16x128_f8f6f4 v[222:225], v[96:103], v[40:47], 0, v143, v143 op_sel_hi:[0,0,0]
	global_load_lds_dwordx4 v138, s[52:53]
	v_mfma_scale_f32_16x16x128_f8f6f4 v[226:229], v[104:111], v[40:47], 0, v143, v143 op_sel_hi:[0,0,0]
	v_mfma_scale_f32_16x16x128_f8f6f4 v[230:233], v[96:103], v[48:55], 0, v143, v143 op_sel_hi:[0,0,0]
	s_mov_b32 m0, s101
	v_mfma_scale_f32_16x16x128_f8f6f4 v[234:237], v[104:111], v[48:55], 0, v143, v143 op_sel_hi:[0,0,0]
	global_load_lds_dwordx4 v139, s[52:53]
	v_mfma_scale_f32_16x16x128_f8f6f4 v[238:241], v[96:103], v[56:63], 0, v143, v143 op_sel_hi:[0,0,0]
	v_mfma_scale_f32_16x16x128_f8f6f4 v[242:245], v[104:111], v[56:63], 0, v143, v143 op_sel_hi:[0,0,0]
	s_setprio 0
	s_add_i32 s51, 0, 0x18000
	s_nop 1
	v_add_u32_e32 v12, s51, v140
	s_barrier
	s_nop 0
	ds_read_b128 v[0:3], v12
	ds_read_b128 v[4:7], v12 offset:1024
	ds_read_b128 v[8:11], v12 offset:2048
	ds_read_b128 v[12:15], v12 offset:3072
	s_add_u32 s52, s24, 0x40000
	v_mov_b32_e32 v40, v138
	ds_read_b128 v[16:19], v142 offset:32768
	ds_read_b128 v[20:23], v142 offset:33792
	ds_read_b128 v[24:27], v142 offset:34816
	ds_read_b128 v[28:31], v142 offset:35840
	ds_read_b128 v[32:35], v142 offset:36864
	ds_read_b128 v[36:39], v142 offset:37888
	ds_read_b128 v[64:67], v142 offset:38912
	ds_read_b128 v[68:71], v142 offset:39936
	s_addc_u32 s53, s25, 0
	s_nop 0
	v_mov_b32_e32 v40, v139
	s_nop 0
	s_waitcnt lgkmcnt(8)
	s_barrier
	s_waitcnt lgkmcnt(0)
	s_setprio 1
	s_waitcnt lgkmcnt(0)
	v_mfma_scale_f32_16x16x128_f8f6f4 v[124:127], v[0:7], v[16:23], v[124:127], v143, v143 op_sel_hi:[0,0,0]
	v_mfma_scale_f32_16x16x128_f8f6f4 v[120:123], v[8:15], v[16:23], v[120:123], v143, v143 op_sel_hi:[0,0,0]
	s_mov_b32 m0, s30
	v_mfma_scale_f32_16x16x128_f8f6f4 v[116:119], v[0:7], v[24:31], v[116:119], v143, v143 op_sel_hi:[0,0,0]
	global_load_lds_dwordx4 v138, s[52:53]
	v_mfma_scale_f32_16x16x128_f8f6f4 v[112:115], v[8:15], v[24:31], v[112:115], v143, v143 op_sel_hi:[0,0,0]
	v_mfma_scale_f32_16x16x128_f8f6f4 v[108:111], v[0:7], v[32:39], v[132:135], v143, v143 op_sel_hi:[0,0,0]
	s_mov_b32 m0, s31
	v_mfma_scale_f32_16x16x128_f8f6f4 v[104:107], v[8:15], v[32:39], v[194:197], v143, v143 op_sel_hi:[0,0,0]
	global_load_lds_dwordx4 v139, s[52:53]
	v_mfma_scale_f32_16x16x128_f8f6f4 v[100:103], v[0:7], v[64:71], v[198:201], v143, v143 op_sel_hi:[0,0,0]
	v_mfma_scale_f32_16x16x128_f8f6f4 v[96:99], v[8:15], v[64:71], v[202:205], v143, v143 op_sel_hi:[0,0,0]
	s_setprio 0
	s_barrier
	s_add_i32 s52, 0, 0x1c000
	v_add_u32_e32 v40, s52, v140
	v_mov_b32_e32 v128, v138
	ds_read_b128 v[146:149], v40
	ds_read_b128 v[150:153], v40 offset:1024
	ds_read_b128 v[154:157], v40 offset:2048
	ds_read_b128 v[158:161], v40 offset:3072
	s_add_i32 s51, s51, s28
	v_lshl_add_u64 v[40:41], s[22:23], 0, v[128:129]
	v_lshl_add_u64 v[40:41], v[40:41], 0, s[6:7]
	v_mov_b32_e32 v128, v139
	v_lshl_add_u64 v[40:41], s[22:23], 0, v[128:129]
	v_lshl_add_u64 v[40:41], v[40:41], 0, s[6:7]
	s_barrier
	s_waitcnt lgkmcnt(0)
	s_setprio 1
	s_waitcnt lgkmcnt(0)
	v_mfma_scale_f32_16x16x128_f8f6f4 v[60:63], v[146:153], v[16:23], v[206:209], v143, v143 op_sel_hi:[0,0,0]
	v_mfma_scale_f32_16x16x128_f8f6f4 v[56:59], v[154:161], v[16:23], v[162:165], v143, v143 op_sel_hi:[0,0,0]
	s_add_u32 s98, s22, s6
	s_addc_u32 s99, s23, s7
	s_mov_b32 m0, s51
	v_mfma_scale_f32_16x16x128_f8f6f4 v[52:55], v[146:153], v[24:31], v[166:169], v143, v143 op_sel_hi:[0,0,0]
	global_load_lds_dwordx4 v138, s[98:99]
	v_mfma_scale_f32_16x16x128_f8f6f4 v[48:51], v[154:161], v[24:31], v[170:173], v143, v143 op_sel_hi:[0,0,0]
	v_mfma_scale_f32_16x16x128_f8f6f4 v[44:47], v[146:153], v[32:39], v[174:177], v143, v143 op_sel_hi:[0,0,0]
	s_add_i32 m0, s51, 0x2000
	v_mfma_scale_f32_16x16x128_f8f6f4 v[40:43], v[154:161], v[32:39], v[178:181], v143, v143 op_sel_hi:[0,0,0]
	global_load_lds_dwordx4 v139, s[98:99]
	v_mfma_scale_f32_16x16x128_f8f6f4 v[36:39], v[146:153], v[64:71], v[182:185], v143, v143 op_sel_hi:[0,0,0]
	v_mfma_scale_f32_16x16x128_f8f6f4 v[32:35], v[154:161], v[64:71], v[186:189], v143, v143 op_sel_hi:[0,0,0]
	s_setprio 0
	v_mov_b32_e32 v128, v138
	s_barrier
	ds_read_b128 v[16:19], v142 offset:49152
	ds_read_b128 v[20:23], v142 offset:50176
	ds_read_b128 v[162:165], v142 offset:51200
	ds_read_b128 v[166:169], v142 offset:52224
	ds_read_b128 v[170:173], v142 offset:53248
	ds_read_b128 v[174:177], v142 offset:54272
	ds_read_b128 v[178:181], v142 offset:55296
	ds_read_b128 v[182:185], v142 offset:56320
	v_lshl_add_u64 v[24:25], s[24:25], 0, v[128:129]
	v_lshl_add_u64 v[24:25], v[24:25], 0, s[6:7]
	v_mov_b32_e32 v128, v139
	v_lshl_add_u64 v[24:25], s[24:25], 0, v[128:129]
	v_lshl_add_u64 v[24:25], v[24:25], 0, s[6:7]
	s_barrier
	s_waitcnt lgkmcnt(0)
	s_setprio 1
	s_waitcnt lgkmcnt(0)
	v_mfma_scale_f32_16x16x128_f8f6f4 v[92:95], v[0:7], v[16:23], v[92:95], v143, v143 op_sel_hi:[0,0,0]
	v_mfma_scale_f32_16x16x128_f8f6f4 v[88:91], v[8:15], v[16:23], v[88:91], v143, v143 op_sel_hi:[0,0,0]
	s_add_u32 s98, s24, s6
	s_addc_u32 s99, s25, s7
	s_mov_b32 m0, s41
	v_mfma_scale_f32_16x16x128_f8f6f4 v[84:87], v[0:7], v[162:169], v[84:87], v143, v143 op_sel_hi:[0,0,0]
	global_load_lds_dwordx4 v138, s[98:99]
	v_mfma_scale_f32_16x16x128_f8f6f4 v[80:83], v[8:15], v[162:169], v[80:83], v143, v143 op_sel_hi:[0,0,0]
	v_mfma_scale_f32_16x16x128_f8f6f4 v[76:79], v[0:7], v[170:177], v[76:79], v143, v143 op_sel_hi:[0,0,0]
	s_mov_b32 m0, s42
	v_mfma_scale_f32_16x16x128_f8f6f4 v[72:75], v[8:15], v[170:177], v[72:75], v143, v143 op_sel_hi:[0,0,0]
	global_load_lds_dwordx4 v139, s[98:99]
	v_mfma_scale_f32_16x16x128_f8f6f4 v[68:71], v[0:7], v[178:185], v[190:193], v143, v143 op_sel_hi:[0,0,0]
	v_mfma_scale_f32_16x16x128_f8f6f4 v[64:67], v[8:15], v[178:185], v[210:213], v143, v143 op_sel_hi:[0,0,0]
	s_setprio 0
	s_barrier
	s_add_u32 s22, s22, 0x40080
	s_addc_u32 s23, s23, 0
	v_mov_b32_e32 v0, v138
	s_add_i32 s24, s52, s28
	s_nop 0
	v_mov_b32_e32 v0, v139
	s_nop 0
	s_waitcnt vmcnt(4)
	s_barrier
	s_setprio 1
	v_mfma_scale_f32_16x16x128_f8f6f4 v[28:31], v[146:153], v[16:23], v[214:217], v143, v143 op_sel_hi:[0,0,0]
	v_mfma_scale_f32_16x16x128_f8f6f4 v[24:27], v[154:161], v[16:23], v[218:221], v143, v143 op_sel_hi:[0,0,0]
	s_mov_b32 m0, s24
	v_mfma_scale_f32_16x16x128_f8f6f4 v[20:23], v[146:153], v[162:169], v[222:225], v143, v143 op_sel_hi:[0,0,0]
	global_load_lds_dwordx4 v138, s[22:23]
	v_mfma_scale_f32_16x16x128_f8f6f4 v[16:19], v[154:161], v[162:169], v[226:229], v143, v143 op_sel_hi:[0,0,0]
	v_mfma_scale_f32_16x16x128_f8f6f4 v[12:15], v[146:153], v[170:177], v[230:233], v143, v143 op_sel_hi:[0,0,0]
	s_add_i32 m0, s24, 0x2000
	v_mfma_scale_f32_16x16x128_f8f6f4 v[8:11], v[154:161], v[170:177], v[234:237], v143, v143 op_sel_hi:[0,0,0]
	global_load_lds_dwordx4 v139, s[22:23]
	v_mfma_scale_f32_16x16x128_f8f6f4 v[4:7], v[146:153], v[178:185], v[238:241], v143, v143 op_sel_hi:[0,0,0]
	v_mfma_scale_f32_16x16x128_f8f6f4 v[0:3], v[154:161], v[178:185], v[242:245], v143, v143 op_sel_hi:[0,0,0]
	s_setprio 0
	s_add_i32 s50, s50, 2
	s_add_u32 s20, s20, 0x100
	s_addc_u32 s21, s21, 0
	s_add_u32 s11, s11, 0x100
	s_addc_u32 s13, s13, 0
	s_cmp_gt_u32 s50, 13
	s_barrier
	s_cbranch_scc0 .LBB0_4932
	s_branch .Lpeel_exit_7
	.p2align 6

.LBB0_5812:
	s_add_u32 s14, s14, 0x30080
	s_addc_u32 s15, s15, 0
	s_add_u32 s51, s16, 0x100
	v_mov_b32_e32 v0, 0
	s_addc_u32 s52, s17, 0
	s_mov_b32 s53, -2
	.p2align 6
.Lpeel_9:
	ds_read_b128 v[140:143], v134
	ds_read_b128 v[144:147], v134 offset:1024
	ds_read_b128 v[148:151], v134 offset:2048
	ds_read_b128 v[152:155], v134 offset:3072
	s_add_u32 s16, s14, 0xfffd0080
	s_addc_u32 s17, s15, -1
	s_cmp_eq_u32 s53, 8
	s_cselect_b32 s19, s13, s17
	s_cselect_b32 s18, s12, s16
	s_cselect_b32 s17, s11, s52
	s_cselect_b32 s16, s10, s51
	v_mov_b32_e32 v128, v132
	ds_read_b128 v[156:159], v135
	ds_read_b128 v[160:163], v135 offset:1024
	ds_read_b128 v[164:167], v135 offset:2048
	ds_read_b128 v[168:171], v135 offset:3072
	ds_read_b128 v[172:175], v135 offset:4096
	ds_read_b128 v[176:179], v135 offset:5120
	ds_read_b128 v[180:183], v135 offset:6144
	ds_read_b128 v[184:187], v135 offset:7168
	s_nop 0
	v_mov_b32_e32 v128, v133
	s_nop 0
	s_waitcnt lgkmcnt(8)
	s_barrier
	s_waitcnt lgkmcnt(0)
	s_setprio 1
	s_waitcnt lgkmcnt(0)
	v_mfma_scale_f32_16x16x128_f8f6f4 v[124:127], v[140:147], v[156:163], 0, v136, v136 op_sel_hi:[0,0,0]
	v_mfma_scale_f32_16x16x128_f8f6f4 v[120:123], v[148:155], v[156:163], 0, v136, v136 op_sel_hi:[0,0,0]
	s_mov_b32 m0, s38
	v_mfma_scale_f32_16x16x128_f8f6f4 v[116:119], v[140:147], v[164:171], 0, v136, v136 op_sel_hi:[0,0,0]
	global_load_lds_dwordx4 v132, s[14:15]
	v_mfma_scale_f32_16x16x128_f8f6f4 v[112:115], v[148:155], v[164:171], 0, v136, v136 op_sel_hi:[0,0,0]
	v_mfma_scale_f32_16x16x128_f8f6f4 v[188:191], v[140:147], v[172:179], 0, v136, v136 op_sel_hi:[0,0,0]
	s_mov_b32 m0, s39
	v_mfma_scale_f32_16x16x128_f8f6f4 v[192:195], v[148:155], v[172:179], 0, v136, v136 op_sel_hi:[0,0,0]
	global_load_lds_dwordx4 v133, s[14:15]
	v_mfma_scale_f32_16x16x128_f8f6f4 v[196:199], v[140:147], v[180:187], 0, v136, v136 op_sel_hi:[0,0,0]
	v_mfma_scale_f32_16x16x128_f8f6f4 v[200:203], v[148:155], v[180:187], 0, v136, v136 op_sel_hi:[0,0,0]
	s_setprio 0
	s_barrier
	v_mov_b32_e32 v128, v132
	s_nop 2
	ds_read_b128 v[96:99], v137
	ds_read_b128 v[100:103], v137 offset:1024
	ds_read_b128 v[104:107], v137 offset:2048
	ds_read_b128 v[108:111], v137 offset:3072
	s_nop 0
	v_mov_b32_e32 v128, v133
	s_nop 0
	s_barrier
	s_waitcnt lgkmcnt(0)
	s_setprio 1
	s_waitcnt lgkmcnt(0)
	v_mfma_scale_f32_16x16x128_f8f6f4 v[204:207], v[96:103], v[156:163], 0, v136, v136 op_sel_hi:[0,0,0]
	v_mfma_scale_f32_16x16x128_f8f6f4 v[156:159], v[104:111], v[156:163], 0, v136, v136 op_sel_hi:[0,0,0]
	s_mov_b32 m0, s40
	v_mfma_scale_f32_16x16x128_f8f6f4 v[160:163], v[96:103], v[164:171], 0, v136, v136 op_sel_hi:[0,0,0]
	global_load_lds_dwordx4 v132, s[16:17]
	v_mfma_scale_f32_16x16x128_f8f6f4 v[164:167], v[104:111], v[164:171], 0, v136, v136 op_sel_hi:[0,0,0]
	v_mfma_scale_f32_16x16x128_f8f6f4 v[168:171], v[96:103], v[172:179], 0, v136, v136 op_sel_hi:[0,0,0]
	s_mov_b32 m0, s41
	v_mfma_scale_f32_16x16x128_f8f6f4 v[172:175], v[104:111], v[172:179], 0, v136, v136 op_sel_hi:[0,0,0]
	global_load_lds_dwordx4 v133, s[16:17]
	v_mfma_scale_f32_16x16x128_f8f6f4 v[176:179], v[96:103], v[180:187], 0, v136, v136 op_sel_hi:[0,0,0]
	v_mfma_scale_f32_16x16x128_f8f6f4 v[180:183], v[104:111], v[180:187], 0, v136, v136 op_sel_hi:[0,0,0]
	s_setprio 0
	v_mov_b32_e32 v128, v132
	s_barrier
	s_nop 2
	ds_read_b128 v[64:67], v135 offset:16384
	ds_read_b128 v[68:71], v135 offset:17408
	ds_read_b128 v[72:75], v135 offset:18432
	ds_read_b128 v[76:79], v135 offset:19456
	ds_read_b128 v[80:83], v135 offset:20480
	ds_read_b128 v[84:87], v135 offset:21504
	ds_read_b128 v[88:91], v135 offset:22528
	ds_read_b128 v[92:95], v135 offset:23552
	s_nop 0
	v_mov_b32_e32 v128, v133
	s_nop 0
	s_barrier
	s_waitcnt lgkmcnt(0)
	s_setprio 1
	s_waitcnt lgkmcnt(0)
	v_mfma_scale_f32_16x16x128_f8f6f4 v[60:63], v[140:147], v[64:71], 0, v136, v136 op_sel_hi:[0,0,0]
	v_mfma_scale_f32_16x16x128_f8f6f4 v[56:59], v[148:155], v[64:71], 0, v136, v136 op_sel_hi:[0,0,0]
	s_mov_b32 m0, s24
	v_mfma_scale_f32_16x16x128_f8f6f4 v[52:55], v[140:147], v[72:79], 0, v136, v136 op_sel_hi:[0,0,0]
	global_load_lds_dwordx4 v132, s[18:19]
	v_mfma_scale_f32_16x16x128_f8f6f4 v[48:51], v[148:155], v[72:79], 0, v136, v136 op_sel_hi:[0,0,0]
	v_mfma_scale_f32_16x16x128_f8f6f4 v[184:187], v[140:147], v[80:87], 0, v136, v136 op_sel_hi:[0,0,0]
	s_mov_b32 m0, s25
	v_mfma_scale_f32_16x16x128_f8f6f4 v[208:211], v[148:155], v[80:87], 0, v136, v136 op_sel_hi:[0,0,0]
	global_load_lds_dwordx4 v133, s[18:19]
	v_mfma_scale_f32_16x16x128_f8f6f4 v[212:215], v[140:147], v[88:95], 0, v136, v136 op_sel_hi:[0,0,0]
	v_mfma_scale_f32_16x16x128_f8f6f4 v[216:219], v[148:155], v[88:95], 0, v136, v136 op_sel_hi:[0,0,0]
	s_setprio 0
	s_barrier
	s_add_u32 s54, s16, 0x30000
	s_nop 3
	v_mov_b32_e32 v32, v132
	s_addc_u32 s55, s17, 0
	s_nop 0
	v_mov_b32_e32 v32, v133
	s_nop 0
	s_waitcnt vmcnt(4)
	s_barrier
	s_setprio 1
	v_mfma_scale_f32_16x16x128_f8f6f4 v[220:223], v[96:103], v[64:71], 0, v136, v136 op_sel_hi:[0,0,0]
	v_mfma_scale_f32_16x16x128_f8f6f4 v[224:227], v[104:111], v[64:71], 0, v136, v136 op_sel_hi:[0,0,0]
	s_mov_b32 m0, s42
	v_mfma_scale_f32_16x16x128_f8f6f4 v[228:231], v[96:103], v[72:79], 0, v136, v136 op_sel_hi:[0,0,0]
	global_load_lds_dwordx4 v132, s[54:55]
	v_mfma_scale_f32_16x16x128_f8f6f4 v[232:235], v[104:111], v[72:79], 0, v136, v136 op_sel_hi:[0,0,0]
	v_mfma_scale_f32_16x16x128_f8f6f4 v[236:239], v[96:103], v[80:87], 0, v136, v136 op_sel_hi:[0,0,0]
	s_mov_b32 m0, s43
	v_mfma_scale_f32_16x16x128_f8f6f4 v[240:243], v[104:111], v[80:87], 0, v136, v136 op_sel_hi:[0,0,0]
	global_load_lds_dwordx4 v133, s[54:55]
	v_mfma_scale_f32_16x16x128_f8f6f4 v[244:247], v[96:103], v[88:95], 0, v136, v136 op_sel_hi:[0,0,0]
	v_mfma_scale_f32_16x16x128_f8f6f4 v[248:251], v[104:111], v[88:95], 0, v136, v136 op_sel_hi:[0,0,0]
	s_setprio 0
	s_barrier
	s_nop 4
	ds_read_b128 v[0:3], v138
	ds_read_b128 v[4:7], v138 offset:1024
	ds_read_b128 v[8:11], v138 offset:2048
	ds_read_b128 v[12:15], v138 offset:3072
	s_add_u32 s54, s18, 0x30000
	v_mov_b32_e32 v64, v132
	ds_read_b128 v[16:19], v135 offset:32768
	ds_read_b128 v[20:23], v135 offset:33792
	ds_read_b128 v[24:27], v135 offset:34816
	ds_read_b128 v[28:31], v135 offset:35840
	ds_read_b128 v[32:35], v135 offset:36864
	ds_read_b128 v[36:39], v135 offset:37888
	ds_read_b128 v[40:43], v135 offset:38912
	ds_read_b128 v[44:47], v135 offset:39936
	s_addc_u32 s55, s19, 0
	s_nop 0
	v_mov_b32_e32 v64, v133
	s_nop 0
	s_waitcnt lgkmcnt(8)
	s_barrier
	s_waitcnt lgkmcnt(0)
	s_setprio 1
	s_waitcnt lgkmcnt(0)
	v_mfma_scale_f32_16x16x128_f8f6f4 v[124:127], v[0:7], v[16:23], v[124:127], v136, v136 op_sel_hi:[0,0,0]
	v_mfma_scale_f32_16x16x128_f8f6f4 v[120:123], v[8:15], v[16:23], v[120:123], v136, v136 op_sel_hi:[0,0,0]
	s_mov_b32 m0, s26
	v_mfma_scale_f32_16x16x128_f8f6f4 v[116:119], v[0:7], v[24:31], v[116:119], v136, v136 op_sel_hi:[0,0,0]
	global_load_lds_dwordx4 v132, s[54:55]
	v_mfma_scale_f32_16x16x128_f8f6f4 v[112:115], v[8:15], v[24:31], v[112:115], v136, v136 op_sel_hi:[0,0,0]
	v_mfma_scale_f32_16x16x128_f8f6f4 v[108:111], v[0:7], v[32:39], v[188:191], v136, v136 op_sel_hi:[0,0,0]
	s_mov_b32 m0, s27
	v_mfma_scale_f32_16x16x128_f8f6f4 v[104:107], v[8:15], v[32:39], v[192:195], v136, v136 op_sel_hi:[0,0,0]
	global_load_lds_dwordx4 v133, s[54:55]
	v_mfma_scale_f32_16x16x128_f8f6f4 v[100:103], v[0:7], v[40:47], v[196:199], v136, v136 op_sel_hi:[0,0,0]
	v_mfma_scale_f32_16x16x128_f8f6f4 v[96:99], v[8:15], v[40:47], v[200:203], v136, v136 op_sel_hi:[0,0,0]
	s_setprio 0
	s_barrier
	v_mov_b32_e32 v128, v132
	ds_read_b128 v[140:143], v139
	ds_read_b128 v[144:147], v139 offset:1024
	ds_read_b128 v[148:151], v139 offset:2048
	ds_read_b128 v[152:155], v139 offset:3072
	v_lshl_add_u64 v[64:65], s[16:17], 0, v[128:129]
	v_lshl_add_u64 v[64:65], v[64:65], 0, s[4:5]
	v_mov_b32_e32 v128, v133
	v_lshl_add_u64 v[64:65], s[16:17], 0, v[128:129]
	v_lshl_add_u64 v[64:65], v[64:65], 0, s[4:5]
	s_barrier
	s_waitcnt lgkmcnt(0)
	s_setprio 1
	s_waitcnt lgkmcnt(0)
	v_mfma_scale_f32_16x16x128_f8f6f4 v[92:95], v[140:147], v[16:23], v[204:207], v136, v136 op_sel_hi:[0,0,0]
	v_mfma_scale_f32_16x16x128_f8f6f4 v[88:91], v[148:155], v[16:23], v[156:159], v136, v136 op_sel_hi:[0,0,0]
	s_add_u32 s98, s16, s4
	s_addc_u32 s99, s17, s5
	s_mov_b32 m0, s45
	v_mfma_scale_f32_16x16x128_f8f6f4 v[84:87], v[140:147], v[24:31], v[160:163], v136, v136 op_sel_hi:[0,0,0]
	global_load_lds_dwordx4 v132, s[98:99]
	v_mfma_scale_f32_16x16x128_f8f6f4 v[80:83], v[148:155], v[24:31], v[164:167], v136, v136 op_sel_hi:[0,0,0]
	v_mfma_scale_f32_16x16x128_f8f6f4 v[76:79], v[140:147], v[32:39], v[168:171], v136, v136 op_sel_hi:[0,0,0]
	s_mov_b32 m0, s46
	v_mfma_scale_f32_16x16x128_f8f6f4 v[72:75], v[148:155], v[32:39], v[172:175], v136, v136 op_sel_hi:[0,0,0]
	global_load_lds_dwordx4 v133, s[98:99]
	v_mfma_scale_f32_16x16x128_f8f6f4 v[68:71], v[140:147], v[40:47], v[176:179], v136, v136 op_sel_hi:[0,0,0]
	v_mfma_scale_f32_16x16x128_f8f6f4 v[64:67], v[148:155], v[40:47], v[180:183], v136, v136 op_sel_hi:[0,0,0]
	s_setprio 0
	v_mov_b32_e32 v128, v132
	s_barrier
	ds_read_b128 v[16:19], v135 offset:49152
	ds_read_b128 v[20:23], v135 offset:50176
	ds_read_b128 v[156:159], v135 offset:51200
	ds_read_b128 v[160:163], v135 offset:52224
	ds_read_b128 v[164:167], v135 offset:53248
	ds_read_b128 v[168:171], v135 offset:54272
	ds_read_b128 v[172:175], v135 offset:55296
	ds_read_b128 v[176:179], v135 offset:56320
	v_lshl_add_u64 v[24:25], s[18:19], 0, v[128:129]
	v_lshl_add_u64 v[24:25], v[24:25], 0, s[4:5]
	v_mov_b32_e32 v128, v133
	v_lshl_add_u64 v[24:25], s[18:19], 0, v[128:129]
	v_lshl_add_u64 v[24:25], v[24:25], 0, s[4:5]
	s_barrier
	s_waitcnt lgkmcnt(0)
	s_setprio 1
	s_waitcnt lgkmcnt(0)
	v_mfma_scale_f32_16x16x128_f8f6f4 v[60:63], v[0:7], v[16:23], v[60:63], v136, v136 op_sel_hi:[0,0,0]
	v_mfma_scale_f32_16x16x128_f8f6f4 v[56:59], v[8:15], v[16:23], v[56:59], v136, v136 op_sel_hi:[0,0,0]
	s_add_u32 s98, s18, s4
	s_addc_u32 s99, s19, s5
	s_mov_b32 m0, s35
	v_mfma_scale_f32_16x16x128_f8f6f4 v[52:55], v[0:7], v[156:163], v[52:55], v136, v136 op_sel_hi:[0,0,0]
	global_load_lds_dwordx4 v132, s[98:99]
	v_mfma_scale_f32_16x16x128_f8f6f4 v[48:51], v[8:15], v[156:163], v[48:51], v136, v136 op_sel_hi:[0,0,0]
	v_mfma_scale_f32_16x16x128_f8f6f4 v[44:47], v[0:7], v[164:171], v[184:187], v136, v136 op_sel_hi:[0,0,0]
	s_mov_b32 m0, s36
	v_mfma_scale_f32_16x16x128_f8f6f4 v[40:43], v[8:15], v[164:171], v[208:211], v136, v136 op_sel_hi:[0,0,0]
	global_load_lds_dwordx4 v133, s[98:99]
	v_mfma_scale_f32_16x16x128_f8f6f4 v[36:39], v[0:7], v[172:179], v[212:215], v136, v136 op_sel_hi:[0,0,0]
	v_mfma_scale_f32_16x16x128_f8f6f4 v[32:35], v[8:15], v[172:179], v[216:219], v136, v136 op_sel_hi:[0,0,0]
	s_setprio 0
	s_barrier
	s_add_u32 s16, s16, 0x30080
	s_addc_u32 s17, s17, 0
	v_mov_b32_e32 v0, v132
	s_add_i32 s18, s44, s23
	s_nop 0
	v_mov_b32_e32 v0, v133
	s_nop 0
	s_waitcnt vmcnt(4)
	s_barrier
	s_setprio 1
	v_mfma_scale_f32_16x16x128_f8f6f4 v[28:31], v[140:147], v[16:23], v[220:223], v136, v136 op_sel_hi:[0,0,0]
	v_mfma_scale_f32_16x16x128_f8f6f4 v[24:27], v[148:155], v[16:23], v[224:227], v136, v136 op_sel_hi:[0,0,0]
	s_mov_b32 m0, s18
	v_mfma_scale_f32_16x16x128_f8f6f4 v[20:23], v[140:147], v[156:163], v[228:231], v136, v136 op_sel_hi:[0,0,0]
	global_load_lds_dwordx4 v132, s[16:17]
	v_mfma_scale_f32_16x16x128_f8f6f4 v[16:19], v[148:155], v[156:163], v[232:235], v136, v136 op_sel_hi:[0,0,0]
	v_mfma_scale_f32_16x16x128_f8f6f4 v[12:15], v[140:147], v[164:171], v[236:239], v136, v136 op_sel_hi:[0,0,0]
	s_add_i32 m0, s18, 0x2000
	v_mfma_scale_f32_16x16x128_f8f6f4 v[8:11], v[148:155], v[164:171], v[240:243], v136, v136 op_sel_hi:[0,0,0]
	global_load_lds_dwordx4 v133, s[16:17]
	v_mfma_scale_f32_16x16x128_f8f6f4 v[4:7], v[140:147], v[172:179], v[244:247], v136, v136 op_sel_hi:[0,0,0]
	v_mfma_scale_f32_16x16x128_f8f6f4 v[0:3], v[148:155], v[172:179], v[248:251], v136, v136 op_sel_hi:[0,0,0]
	s_setprio 0
	s_add_i32 s53, s53, 2
	s_add_u32 s14, s14, 0x100
	s_addc_u32 s15, s15, 0
	s_add_u32 s51, s51, 0x100
	s_addc_u32 s52, s52, 0
	s_cmp_gt_u32 s53, 9
	s_barrier
	s_cbranch_scc0 .LBB0_5813
	s_branch .Lpeel_exit_9
	.p2align 6
